# speedup vs baseline: 1.0181x; 1.0181x over previous
.Lrs_a_4:
	s_add_u32 s81, s40, s22
	s_addc_u32 s82, s41, s23
	s_add_u32 s29, s40, 0x100
	s_addc_u32 s44, s41, 0
	s_and_b64 s[42:43], s[14:15], exec
	ds_read_b128 v[82:85], v161
	ds_read_b128 v[94:97], v161 offset:2048
	ds_read_b128 v[102:105], v162
	ds_read_b128 v[110:113], v162 offset:2048
	s_cselect_b32 s47, s37, s44
	s_cselect_b32 s46, s36, s29
	s_add_u32 s29, s38, 0x100
	s_addc_u32 s44, s39, 0
	s_and_b64 s[42:43], s[14:15], exec
	s_cselect_b32 s49, s5, s44
	s_cselect_b32 s48, s4, s29
	s_add_u32 s44, s46, 0x80
	s_addc_u32 s45, s47, 0
	s_add_u32 s42, s48, 0x80
	s_addc_u32 s43, s49, 0
	ds_read_b128 v[58:61], v163
	ds_read_b128 v[66:69], v163 offset:2048
	ds_read_b128 v[62:65], v164
	ds_read_b128 v[70:73], v164 offset:2048
	ds_read_b128 v[74:77], v163 offset:4096
	ds_read_b128 v[86:89], v163 offset:6144
	ds_read_b128 v[78:81], v164 offset:4096
	ds_read_b128 v[90:93], v164 offset:6144
	s_add_u32 s78, s81, 0x80
	s_addc_u32 s79, s82, 0
	s_mov_b32 m0, s70
	s_nop 0
	global_load_lds_dwordx4 v146, s[78:79]
	s_mov_b32 m0, s71
	s_nop 0
	global_load_lds_dwordx4 v150, s[78:79]
	s_waitcnt lgkmcnt(8)
	ds_read_b128 v[142:145], v161 offset:16384
	ds_read_b128 v[166:169], v161 offset:18432
	ds_read_b128 v[170:173], v162 offset:16384
	ds_read_b128 v[174:177], v162 offset:18432
	s_waitcnt vmcnt(8)
	s_waitcnt lgkmcnt(0)
	s_barrier
	s_waitcnt lgkmcnt(0)
	s_waitcnt vmcnt(16)
	v_mov_b32_e32 v1, v0
	v_pk_mul_f32 v[16:17], v[0:1], v[16:17]
	v_pk_mul_f32 v[14:15], v[154:155], v[14:15]
	v_pk_mul_f32 v[12:13], v[0:1], v[12:13]
	v_pk_mul_f32 v[10:11], v[154:155], v[10:11]
	v_pk_mul_f32 v[8:9], v[0:1], v[8:9]
	v_pk_mul_f32 v[6:7], v[154:155], v[6:7]
	v_pk_mul_f32 v[4:5], v[0:1], v[4:5]
	v_pk_mul_f32 v[2:3], v[154:155], v[2:3]
	s_setprio 1
	v_mfma_f32_16x16x128_f8f6f4 v[18:21], v[82:85], v[58:61], v[14:17] cbsz:4 blgp:4
	v_mfma_f32_16x16x128_f8f6f4 v[18:21], v[102:105], v[62:65], v[18:21] cbsz:4 blgp:4
	v_mfma_f32_16x16x128_f8f6f4 v[22:25], v[94:97], v[58:61], v[10:13] cbsz:4 blgp:4
	v_mfma_f32_16x16x128_f8f6f4 v[22:25], v[110:113], v[62:65], v[22:25] cbsz:4 blgp:4
	v_mfma_f32_16x16x128_f8f6f4 v[26:29], v[82:85], v[66:69], v[14:17] cbsz:4 blgp:4
	v_mfma_f32_16x16x128_f8f6f4 v[26:29], v[102:105], v[70:73], v[26:29] cbsz:4 blgp:4
	v_mfma_f32_16x16x128_f8f6f4 v[30:33], v[94:97], v[66:69], v[10:13] cbsz:4 blgp:4
	v_mfma_f32_16x16x128_f8f6f4 v[30:33], v[110:113], v[70:73], v[30:33] cbsz:4 blgp:4
	v_mfma_f32_16x16x128_f8f6f4 v[34:37], v[82:85], v[74:77], v[14:17] cbsz:4 blgp:4
	v_mfma_f32_16x16x128_f8f6f4 v[34:37], v[102:105], v[78:81], v[34:37] cbsz:4 blgp:4
	v_mfma_f32_16x16x128_f8f6f4 v[38:41], v[94:97], v[74:77], v[10:13] cbsz:4 blgp:4
	v_mfma_f32_16x16x128_f8f6f4 v[38:41], v[110:113], v[78:81], v[38:41] cbsz:4 blgp:4
	v_mfma_f32_16x16x128_f8f6f4 v[42:45], v[82:85], v[86:89], v[14:17] cbsz:4 blgp:4
	v_mfma_f32_16x16x128_f8f6f4 v[42:45], v[102:105], v[90:93], v[42:45] cbsz:4 blgp:4
	v_mfma_f32_16x16x128_f8f6f4 v[46:49], v[94:97], v[86:89], v[10:13] cbsz:4 blgp:4
	v_mfma_f32_16x16x128_f8f6f4 v[46:49], v[110:113], v[90:93], v[46:49] cbsz:4 blgp:4
	v_mfma_f32_16x16x128_f8f6f4 v[50:53], v[142:145], v[58:61], v[6:9] cbsz:4 blgp:4
	v_mfma_f32_16x16x128_f8f6f4 v[50:53], v[170:173], v[62:65], v[50:53] cbsz:4 blgp:4
	v_mfma_f32_16x16x128_f8f6f4 v[54:57], v[166:169], v[58:61], v[2:5] cbsz:4 blgp:4
	v_mfma_f32_16x16x128_f8f6f4 v[54:57], v[174:177], v[62:65], v[54:57] cbsz:4 blgp:4
	v_mfma_f32_16x16x128_f8f6f4 v[58:61], v[142:145], v[66:69], v[6:9] cbsz:4 blgp:4
	v_mfma_f32_16x16x128_f8f6f4 v[58:61], v[170:173], v[70:73], v[58:61] cbsz:4 blgp:4
	v_mfma_f32_16x16x128_f8f6f4 v[62:65], v[166:169], v[66:69], v[2:5] cbsz:4 blgp:4
	v_mfma_f32_16x16x128_f8f6f4 v[62:65], v[174:177], v[70:73], v[62:65] cbsz:4 blgp:4
	v_mfma_f32_16x16x128_f8f6f4 v[66:69], v[142:145], v[74:77], v[6:9] cbsz:4 blgp:4
	v_mfma_f32_16x16x128_f8f6f4 v[66:69], v[170:173], v[78:81], v[66:69] cbsz:4 blgp:4
	v_mfma_f32_16x16x128_f8f6f4 v[70:73], v[166:169], v[74:77], v[2:5] cbsz:4 blgp:4
	v_mfma_f32_16x16x128_f8f6f4 v[70:73], v[174:177], v[78:81], v[70:73] cbsz:4 blgp:4
	v_mfma_f32_16x16x128_f8f6f4 v[74:77], v[142:145], v[86:89], v[6:9] cbsz:4 blgp:4
	v_mfma_f32_16x16x128_f8f6f4 v[74:77], v[170:173], v[90:93], v[74:77] cbsz:4 blgp:4
	v_mfma_f32_16x16x128_f8f6f4 v[78:81], v[166:169], v[86:89], v[2:5] cbsz:4 blgp:4
	v_mfma_f32_16x16x128_f8f6f4 v[78:81], v[174:177], v[90:93], v[78:81] cbsz:4 blgp:4
	s_setprio 0
	s_barrier
	s_mov_b32 m0, s55
	s_nop 0
	global_load_lds_dwordx4 v148, s[48:49]
	s_mov_b32 m0, s56
	s_nop 0
	global_load_lds_dwordx4 v152, s[48:49]
	ds_read_b128 v[114:117], v163 offset:16384
	ds_read_b128 v[122:125], v163 offset:18432
	ds_read_b128 v[130:133], v164 offset:16384
	ds_read_b128 v[134:137], v164 offset:18432
	ds_read_b128 v[178:181], v163 offset:20480
	ds_read_b128 v[182:185], v163 offset:22528
	ds_read_b128 v[186:189], v164 offset:20480
	ds_read_b128 v[190:193], v164 offset:22528
	s_mov_b32 m0, s54
	s_nop 0
	global_load_lds_dwordx4 v146, s[46:47]
	s_mov_b32 m0, s57
	s_nop 0
	global_load_lds_dwordx4 v150, s[46:47]
	s_add_u32 s48, s48, s24
	s_addc_u32 s49, s49, s25
	s_mov_b32 m0, s58
	s_nop 0
	global_load_lds_dwordx4 v148, s[48:49]
	s_mov_b32 m0, s59
	s_nop 0
	global_load_lds_dwordx4 v152, s[48:49]
	s_waitcnt vmcnt(8)
	s_waitcnt lgkmcnt(0)
	s_barrier
	s_setprio 1
	v_mfma_f32_16x16x128_f8f6f4 v[86:89], v[82:85], v[114:117], v[14:17] cbsz:4 blgp:4
	v_mfma_f32_16x16x128_f8f6f4 v[86:89], v[102:105], v[130:133], v[86:89] cbsz:4 blgp:4
	v_mfma_f32_16x16x128_f8f6f4 v[90:93], v[94:97], v[114:117], v[10:13] cbsz:4 blgp:4
	v_mfma_f32_16x16x128_f8f6f4 v[90:93], v[110:113], v[130:133], v[90:93] cbsz:4 blgp:4
	v_mfma_f32_16x16x128_f8f6f4 v[98:101], v[82:85], v[122:125], v[14:17] cbsz:4 blgp:4
	v_mfma_f32_16x16x128_f8f6f4 v[98:101], v[102:105], v[134:137], v[98:101] cbsz:4 blgp:4
	v_mfma_f32_16x16x128_f8f6f4 v[106:109], v[94:97], v[122:125], v[10:13] cbsz:4 blgp:4
	v_mfma_f32_16x16x128_f8f6f4 v[106:109], v[110:113], v[134:137], v[106:109] cbsz:4 blgp:4
	v_mfma_f32_16x16x128_f8f6f4 v[118:121], v[82:85], v[178:181], v[14:17] cbsz:4 blgp:4
	v_mfma_f32_16x16x128_f8f6f4 v[118:121], v[102:105], v[186:189], v[118:121] cbsz:4 blgp:4
	v_mfma_f32_16x16x128_f8f6f4 v[126:129], v[94:97], v[178:181], v[10:13] cbsz:4 blgp:4
	v_mfma_f32_16x16x128_f8f6f4 v[126:129], v[110:113], v[186:189], v[126:129] cbsz:4 blgp:4
	v_mfma_f32_16x16x128_f8f6f4 v[138:141], v[82:85], v[182:185], v[14:17] cbsz:4 blgp:4
	v_mfma_f32_16x16x128_f8f6f4 v[138:141], v[102:105], v[190:193], v[138:141] cbsz:4 blgp:4
	v_mfma_f32_16x16x128_f8f6f4 v[82:85], v[94:97], v[182:185], v[10:13] cbsz:4 blgp:4
	v_mfma_f32_16x16x128_f8f6f4 v[82:85], v[110:113], v[190:193], v[82:85] cbsz:4 blgp:4
	v_mfma_f32_16x16x128_f8f6f4 v[94:97], v[142:145], v[114:117], v[6:9] cbsz:4 blgp:4
	v_mfma_f32_16x16x128_f8f6f4 v[94:97], v[170:173], v[130:133], v[94:97] cbsz:4 blgp:4
	v_mfma_f32_16x16x128_f8f6f4 v[102:105], v[166:169], v[114:117], v[2:5] cbsz:4 blgp:4
	v_mfma_f32_16x16x128_f8f6f4 v[102:105], v[174:177], v[130:133], v[102:105] cbsz:4 blgp:4
	v_mfma_f32_16x16x128_f8f6f4 v[110:113], v[142:145], v[122:125], v[6:9] cbsz:4 blgp:4
	v_mfma_f32_16x16x128_f8f6f4 v[110:113], v[170:173], v[134:137], v[110:113] cbsz:4 blgp:4
	v_mfma_f32_16x16x128_f8f6f4 v[114:117], v[166:169], v[122:125], v[2:5] cbsz:4 blgp:4
	v_mfma_f32_16x16x128_f8f6f4 v[114:117], v[174:177], v[134:137], v[114:117] cbsz:4 blgp:4
	v_mfma_f32_16x16x128_f8f6f4 v[122:125], v[142:145], v[178:181], v[6:9] cbsz:4 blgp:4
	v_mfma_f32_16x16x128_f8f6f4 v[122:125], v[170:173], v[186:189], v[122:125] cbsz:4 blgp:4
	v_mfma_f32_16x16x128_f8f6f4 v[130:133], v[166:169], v[178:181], v[2:5] cbsz:4 blgp:4
	v_mfma_f32_16x16x128_f8f6f4 v[130:133], v[174:177], v[186:189], v[130:133] cbsz:4 blgp:4
	v_mfma_f32_16x16x128_f8f6f4 v[134:137], v[142:145], v[182:185], v[6:9] cbsz:4 blgp:4
	v_mfma_f32_16x16x128_f8f6f4 v[134:137], v[170:173], v[190:193], v[134:137] cbsz:4 blgp:4
	v_mfma_f32_16x16x128_f8f6f4 v[142:145], v[166:169], v[182:185], v[2:5] cbsz:4 blgp:4
	v_mfma_f32_16x16x128_f8f6f4 v[142:145], v[174:177], v[190:193], v[142:145] cbsz:4 blgp:4
	s_setprio 0
	s_barrier
	ds_read_b128 v[166:169], v161 offset:32768
	ds_read_b128 v[170:173], v161 offset:34816
	ds_read_b128 v[174:177], v162 offset:32768
	ds_read_b128 v[178:181], v162 offset:34816
	ds_read_b128 v[182:185], v163 offset:32768
	ds_read_b128 v[186:189], v163 offset:34816
	ds_read_b128 v[190:193], v164 offset:32768
	ds_read_b128 v[194:197], v164 offset:34816
	ds_read_b128 v[198:201], v163 offset:36864
	ds_read_b128 v[202:205], v163 offset:38912
	ds_read_b128 v[206:209], v164 offset:36864
	ds_read_b128 v[210:213], v164 offset:38912
	s_add_u32 s46, s46, s22
	s_addc_u32 s47, s47, s23
	s_mov_b32 m0, s60
	s_nop 0
	global_load_lds_dwordx4 v146, s[46:47]
	s_mov_b32 m0, s61
	s_nop 0
	global_load_lds_dwordx4 v150, s[46:47]
	s_waitcnt lgkmcnt(8)
	ds_read_b128 v[214:217], v161 offset:49152
	ds_read_b128 v[218:221], v161 offset:51200
	ds_read_b128 v[222:225], v162 offset:49152
	ds_read_b128 v[226:229], v162 offset:51200
	s_waitcnt vmcnt(8)
	s_waitcnt lgkmcnt(0)
	s_barrier
	s_waitcnt lgkmcnt(0)
	s_setprio 1
	v_mfma_f32_16x16x128_f8f6f4 v[18:21], v[166:169], v[182:185], v[18:21] cbsz:4 blgp:4
	v_mfma_f32_16x16x128_f8f6f4 v[18:21], v[174:177], v[190:193], v[18:21] cbsz:4 blgp:4
	v_mfma_f32_16x16x128_f8f6f4 v[22:25], v[170:173], v[182:185], v[22:25] cbsz:4 blgp:4
	v_mfma_f32_16x16x128_f8f6f4 v[22:25], v[178:181], v[190:193], v[22:25] cbsz:4 blgp:4
	v_mfma_f32_16x16x128_f8f6f4 v[26:29], v[166:169], v[186:189], v[26:29] cbsz:4 blgp:4
	v_mfma_f32_16x16x128_f8f6f4 v[26:29], v[174:177], v[194:197], v[26:29] cbsz:4 blgp:4
	v_mfma_f32_16x16x128_f8f6f4 v[30:33], v[170:173], v[186:189], v[30:33] cbsz:4 blgp:4
	v_mfma_f32_16x16x128_f8f6f4 v[30:33], v[178:181], v[194:197], v[30:33] cbsz:4 blgp:4
	v_mfma_f32_16x16x128_f8f6f4 v[34:37], v[166:169], v[198:201], v[34:37] cbsz:4 blgp:4
	v_mfma_f32_16x16x128_f8f6f4 v[34:37], v[174:177], v[206:209], v[34:37] cbsz:4 blgp:4
	v_mfma_f32_16x16x128_f8f6f4 v[38:41], v[170:173], v[198:201], v[38:41] cbsz:4 blgp:4
	v_mfma_f32_16x16x128_f8f6f4 v[38:41], v[178:181], v[206:209], v[38:41] cbsz:4 blgp:4
	v_mfma_f32_16x16x128_f8f6f4 v[42:45], v[166:169], v[202:205], v[42:45] cbsz:4 blgp:4
	v_mfma_f32_16x16x128_f8f6f4 v[42:45], v[174:177], v[210:213], v[42:45] cbsz:4 blgp:4
	v_mfma_f32_16x16x128_f8f6f4 v[46:49], v[170:173], v[202:205], v[46:49] cbsz:4 blgp:4
	v_mfma_f32_16x16x128_f8f6f4 v[46:49], v[178:181], v[210:213], v[46:49] cbsz:4 blgp:4
	v_mfma_f32_16x16x128_f8f6f4 v[50:53], v[214:217], v[182:185], v[50:53] cbsz:4 blgp:4
	v_mfma_f32_16x16x128_f8f6f4 v[50:53], v[222:225], v[190:193], v[50:53] cbsz:4 blgp:4
	v_mfma_f32_16x16x128_f8f6f4 v[54:57], v[218:221], v[182:185], v[54:57] cbsz:4 blgp:4
	v_mfma_f32_16x16x128_f8f6f4 v[54:57], v[226:229], v[190:193], v[54:57] cbsz:4 blgp:4
	v_mfma_f32_16x16x128_f8f6f4 v[58:61], v[214:217], v[186:189], v[58:61] cbsz:4 blgp:4
	v_mfma_f32_16x16x128_f8f6f4 v[58:61], v[222:225], v[194:197], v[58:61] cbsz:4 blgp:4
	v_mfma_f32_16x16x128_f8f6f4 v[62:65], v[218:221], v[186:189], v[62:65] cbsz:4 blgp:4
	v_mfma_f32_16x16x128_f8f6f4 v[62:65], v[226:229], v[194:197], v[62:65] cbsz:4 blgp:4
	v_mfma_f32_16x16x128_f8f6f4 v[66:69], v[214:217], v[198:201], v[66:69] cbsz:4 blgp:4
	v_mfma_f32_16x16x128_f8f6f4 v[66:69], v[222:225], v[206:209], v[66:69] cbsz:4 blgp:4
	v_mfma_f32_16x16x128_f8f6f4 v[70:73], v[218:221], v[198:201], v[70:73] cbsz:4 blgp:4
	v_mfma_f32_16x16x128_f8f6f4 v[70:73], v[226:229], v[206:209], v[70:73] cbsz:4 blgp:4
	v_mfma_f32_16x16x128_f8f6f4 v[74:77], v[214:217], v[202:205], v[74:77] cbsz:4 blgp:4
	v_mfma_f32_16x16x128_f8f6f4 v[74:77], v[222:225], v[210:213], v[74:77] cbsz:4 blgp:4
	v_mfma_f32_16x16x128_f8f6f4 v[78:81], v[218:221], v[202:205], v[78:81] cbsz:4 blgp:4
	v_mfma_f32_16x16x128_f8f6f4 v[78:81], v[226:229], v[210:213], v[78:81] cbsz:4 blgp:4
	s_setprio 0
	s_barrier
	s_mov_b32 m0, s64
	s_nop 0
	global_load_lds_dwordx4 v148, s[42:43]
	s_mov_b32 m0, s65
	s_nop 0
	global_load_lds_dwordx4 v152, s[42:43]
	ds_read_b128 v[182:185], v163 offset:49152
	ds_read_b128 v[186:189], v163 offset:51200
	ds_read_b128 v[190:193], v164 offset:49152
	ds_read_b128 v[194:197], v164 offset:51200
	ds_read_b128 v[198:201], v163 offset:53248
	ds_read_b128 v[202:205], v163 offset:55296
	ds_read_b128 v[206:209], v164 offset:53248
	ds_read_b128 v[210:213], v164 offset:55296
	s_mov_b32 m0, s66
	s_nop 0
	global_load_lds_dwordx4 v146, s[44:45]
	s_mov_b32 m0, s67
	s_nop 0
	global_load_lds_dwordx4 v150, s[44:45]
	s_add_u32 s42, s42, s24
	s_addc_u32 s43, s43, s25
	s_mov_b32 m0, s68
	s_nop 0
	global_load_lds_dwordx4 v148, s[42:43]
	s_mov_b32 m0, s69
	s_nop 0
	global_load_lds_dwordx4 v152, s[42:43]
	s_waitcnt vmcnt(8)
	s_waitcnt lgkmcnt(0)
	s_barrier
	s_setprio 1
	v_mfma_f32_16x16x128_f8f6f4 v[86:89], v[166:169], v[182:185], v[86:89] cbsz:4 blgp:4
	v_mfma_f32_16x16x128_f8f6f4 v[86:89], v[174:177], v[190:193], v[86:89] cbsz:4 blgp:4
	v_mfma_f32_16x16x128_f8f6f4 v[90:93], v[170:173], v[182:185], v[90:93] cbsz:4 blgp:4
	v_mfma_f32_16x16x128_f8f6f4 v[90:93], v[178:181], v[190:193], v[90:93] cbsz:4 blgp:4
	v_mfma_f32_16x16x128_f8f6f4 v[98:101], v[166:169], v[186:189], v[98:101] cbsz:4 blgp:4
	v_mfma_f32_16x16x128_f8f6f4 v[98:101], v[174:177], v[194:197], v[98:101] cbsz:4 blgp:4
	v_mfma_f32_16x16x128_f8f6f4 v[106:109], v[170:173], v[186:189], v[106:109] cbsz:4 blgp:4
	v_mfma_f32_16x16x128_f8f6f4 v[106:109], v[178:181], v[194:197], v[106:109] cbsz:4 blgp:4
	v_mfma_f32_16x16x128_f8f6f4 v[118:121], v[166:169], v[198:201], v[118:121] cbsz:4 blgp:4
	v_mfma_f32_16x16x128_f8f6f4 v[118:121], v[174:177], v[206:209], v[118:121] cbsz:4 blgp:4
	v_mfma_f32_16x16x128_f8f6f4 v[126:129], v[170:173], v[198:201], v[126:129] cbsz:4 blgp:4
	v_mfma_f32_16x16x128_f8f6f4 v[126:129], v[178:181], v[206:209], v[126:129] cbsz:4 blgp:4
	v_mfma_f32_16x16x128_f8f6f4 v[138:141], v[166:169], v[202:205], v[138:141] cbsz:4 blgp:4
	v_mfma_f32_16x16x128_f8f6f4 v[138:141], v[174:177], v[210:213], v[138:141] cbsz:4 blgp:4
	v_mfma_f32_16x16x128_f8f6f4 v[82:85], v[170:173], v[202:205], v[82:85] cbsz:4 blgp:4
	v_mfma_f32_16x16x128_f8f6f4 v[82:85], v[178:181], v[210:213], v[82:85] cbsz:4 blgp:4
	v_mfma_f32_16x16x128_f8f6f4 v[94:97], v[214:217], v[182:185], v[94:97] cbsz:4 blgp:4
	v_mfma_f32_16x16x128_f8f6f4 v[94:97], v[222:225], v[190:193], v[94:97] cbsz:4 blgp:4
	v_mfma_f32_16x16x128_f8f6f4 v[102:105], v[218:221], v[182:185], v[102:105] cbsz:4 blgp:4
	v_mfma_f32_16x16x128_f8f6f4 v[102:105], v[226:229], v[190:193], v[102:105] cbsz:4 blgp:4
	v_mfma_f32_16x16x128_f8f6f4 v[110:113], v[214:217], v[186:189], v[110:113] cbsz:4 blgp:4
	v_mfma_f32_16x16x128_f8f6f4 v[110:113], v[222:225], v[194:197], v[110:113] cbsz:4 blgp:4
	v_mfma_f32_16x16x128_f8f6f4 v[114:117], v[218:221], v[186:189], v[114:117] cbsz:4 blgp:4
	v_mfma_f32_16x16x128_f8f6f4 v[114:117], v[226:229], v[194:197], v[114:117] cbsz:4 blgp:4
	v_mfma_f32_16x16x128_f8f6f4 v[122:125], v[214:217], v[198:201], v[122:125] cbsz:4 blgp:4
	v_mfma_f32_16x16x128_f8f6f4 v[122:125], v[222:225], v[206:209], v[122:125] cbsz:4 blgp:4
	v_mfma_f32_16x16x128_f8f6f4 v[130:133], v[218:221], v[198:201], v[130:133] cbsz:4 blgp:4
	v_mfma_f32_16x16x128_f8f6f4 v[130:133], v[226:229], v[206:209], v[130:133] cbsz:4 blgp:4
	v_mfma_f32_16x16x128_f8f6f4 v[134:137], v[214:217], v[202:205], v[134:137] cbsz:4 blgp:4
	v_mfma_f32_16x16x128_f8f6f4 v[134:137], v[222:225], v[210:213], v[134:137] cbsz:4 blgp:4
	v_mfma_f32_16x16x128_f8f6f4 v[142:145], v[218:221], v[202:205], v[142:145] cbsz:4 blgp:4
	v_mfma_f32_16x16x128_f8f6f4 v[142:145], v[226:229], v[210:213], v[142:145] cbsz:4 blgp:4
	s_setprio 0
	s_andn2_b64 vcc, exec, s[34:35]
	s_barrier
	s_cbranch_vccnz .LBB4_4
	s_ashr_i32 s29, s28, 31
	s_lshl_b64 s[42:43], s[28:29], 10
	s_add_u32 s42, s10, s42
	s_addc_u32 s43, s11, s43
	s_add_u32 s29, s40, 0x200
	s_addc_u32 s78, s41, 0
	s_add_u32 s79, s38, 0x200
	s_addc_u32 s80, s39, 0
	s_add_u32 s38, s81, 0x180
	s_addc_u32 s39, s82, 0
	s_mov_b32 s81, 4
	s_cmp_eq_u32 s63, s81
	s_cselect_b64 s[40:41], -1, 0
	s_cmp_lg_u32 s63, s81
	s_cbranch_scc1 .LBB4_15

.LBB4_15:
	ds_read_b128 v[166:169], v161
	ds_read_b128 v[170:173], v161 offset:2048
	ds_read_b128 v[174:177], v162
	ds_read_b128 v[178:181], v162 offset:2048
	s_and_b64 s[40:41], s[40:41], exec
	s_cselect_b32 s46, s36, s29
	s_cselect_b32 s47, s37, s78
	s_cselect_b32 s49, s5, s80
	s_cselect_b32 s48, s4, s79
	s_add_u32 s44, s46, 0x80
	s_addc_u32 s45, s47, 0
	s_add_u32 s40, s48, 0x80
	s_addc_u32 s41, s49, 0
	ds_read_b128 v[182:185], v163
	ds_read_b128 v[186:189], v163 offset:2048
	ds_read_b128 v[190:193], v164
	ds_read_b128 v[194:197], v164 offset:2048
	ds_read_b128 v[198:201], v163 offset:4096
	ds_read_b128 v[202:205], v163 offset:6144
	ds_read_b128 v[206:209], v164 offset:4096
	ds_read_b128 v[210:213], v164 offset:6144
	s_mov_b32 m0, s70
	s_nop 0
	global_load_lds_dwordx4 v146, s[38:39]
	s_mov_b32 m0, s71
	s_nop 0
	global_load_lds_dwordx4 v150, s[38:39]
	s_waitcnt lgkmcnt(8)
	ds_read_b128 v[214:217], v161 offset:16384
	ds_read_b128 v[218:221], v161 offset:18432
	ds_read_b128 v[222:225], v162 offset:16384
	ds_read_b128 v[226:229], v162 offset:18432
	s_waitcnt vmcnt(8)
	s_waitcnt lgkmcnt(0)
	s_barrier
	s_waitcnt lgkmcnt(0)
	s_setprio 1
	v_mfma_f32_16x16x128_f8f6f4 v[18:21], v[166:169], v[182:185], v[18:21] cbsz:4 blgp:4
	v_mfma_f32_16x16x128_f8f6f4 v[18:21], v[174:177], v[190:193], v[18:21] cbsz:4 blgp:4
	v_mfma_f32_16x16x128_f8f6f4 v[22:25], v[170:173], v[182:185], v[22:25] cbsz:4 blgp:4
	v_mfma_f32_16x16x128_f8f6f4 v[22:25], v[178:181], v[190:193], v[22:25] cbsz:4 blgp:4
	v_mfma_f32_16x16x128_f8f6f4 v[26:29], v[166:169], v[186:189], v[26:29] cbsz:4 blgp:4
	v_mfma_f32_16x16x128_f8f6f4 v[26:29], v[174:177], v[194:197], v[26:29] cbsz:4 blgp:4
	v_mfma_f32_16x16x128_f8f6f4 v[30:33], v[170:173], v[186:189], v[30:33] cbsz:4 blgp:4
	v_mfma_f32_16x16x128_f8f6f4 v[30:33], v[178:181], v[194:197], v[30:33] cbsz:4 blgp:4
	v_mfma_f32_16x16x128_f8f6f4 v[34:37], v[166:169], v[198:201], v[34:37] cbsz:4 blgp:4
	v_mfma_f32_16x16x128_f8f6f4 v[34:37], v[174:177], v[206:209], v[34:37] cbsz:4 blgp:4
	v_mfma_f32_16x16x128_f8f6f4 v[38:41], v[170:173], v[198:201], v[38:41] cbsz:4 blgp:4
	v_mfma_f32_16x16x128_f8f6f4 v[38:41], v[178:181], v[206:209], v[38:41] cbsz:4 blgp:4
	v_mfma_f32_16x16x128_f8f6f4 v[42:45], v[166:169], v[202:205], v[42:45] cbsz:4 blgp:4
	v_mfma_f32_16x16x128_f8f6f4 v[42:45], v[174:177], v[210:213], v[42:45] cbsz:4 blgp:4
	v_mfma_f32_16x16x128_f8f6f4 v[46:49], v[170:173], v[202:205], v[46:49] cbsz:4 blgp:4
	v_mfma_f32_16x16x128_f8f6f4 v[46:49], v[178:181], v[210:213], v[46:49] cbsz:4 blgp:4
	v_mfma_f32_16x16x128_f8f6f4 v[50:53], v[214:217], v[182:185], v[50:53] cbsz:4 blgp:4
	v_mfma_f32_16x16x128_f8f6f4 v[50:53], v[222:225], v[190:193], v[50:53] cbsz:4 blgp:4
	v_mfma_f32_16x16x128_f8f6f4 v[54:57], v[218:221], v[182:185], v[54:57] cbsz:4 blgp:4
	v_mfma_f32_16x16x128_f8f6f4 v[54:57], v[226:229], v[190:193], v[54:57] cbsz:4 blgp:4
	v_mfma_f32_16x16x128_f8f6f4 v[58:61], v[214:217], v[186:189], v[58:61] cbsz:4 blgp:4
	v_mfma_f32_16x16x128_f8f6f4 v[58:61], v[222:225], v[194:197], v[58:61] cbsz:4 blgp:4
	v_mfma_f32_16x16x128_f8f6f4 v[62:65], v[218:221], v[186:189], v[62:65] cbsz:4 blgp:4
	v_mfma_f32_16x16x128_f8f6f4 v[62:65], v[226:229], v[194:197], v[62:65] cbsz:4 blgp:4
	v_mfma_f32_16x16x128_f8f6f4 v[66:69], v[214:217], v[198:201], v[66:69] cbsz:4 blgp:4
	v_mfma_f32_16x16x128_f8f6f4 v[66:69], v[222:225], v[206:209], v[66:69] cbsz:4 blgp:4
	v_mfma_f32_16x16x128_f8f6f4 v[70:73], v[218:221], v[198:201], v[70:73] cbsz:4 blgp:4
	v_mfma_f32_16x16x128_f8f6f4 v[70:73], v[226:229], v[206:209], v[70:73] cbsz:4 blgp:4
	v_mfma_f32_16x16x128_f8f6f4 v[74:77], v[214:217], v[202:205], v[74:77] cbsz:4 blgp:4
	v_mfma_f32_16x16x128_f8f6f4 v[74:77], v[222:225], v[210:213], v[74:77] cbsz:4 blgp:4
	v_mfma_f32_16x16x128_f8f6f4 v[78:81], v[218:221], v[202:205], v[78:81] cbsz:4 blgp:4
	v_mfma_f32_16x16x128_f8f6f4 v[78:81], v[226:229], v[210:213], v[78:81] cbsz:4 blgp:4
	s_setprio 0
	s_barrier
	s_mov_b32 m0, s55
	s_nop 0
	global_load_lds_dwordx4 v148, s[48:49]
	s_mov_b32 m0, s56
	s_nop 0
	global_load_lds_dwordx4 v152, s[48:49]
	ds_read_b128 v[182:185], v163 offset:16384
	ds_read_b128 v[186:189], v163 offset:18432
	ds_read_b128 v[190:193], v164 offset:16384
	ds_read_b128 v[194:197], v164 offset:18432
	ds_read_b128 v[198:201], v163 offset:20480
	ds_read_b128 v[202:205], v163 offset:22528
	ds_read_b128 v[206:209], v164 offset:20480
	ds_read_b128 v[210:213], v164 offset:22528
	s_mov_b32 m0, s54
	s_nop 0
	global_load_lds_dwordx4 v146, s[46:47]
	s_mov_b32 m0, s57
	s_nop 0
	global_load_lds_dwordx4 v150, s[46:47]
	s_add_u32 s48, s48, s24
	s_addc_u32 s49, s49, s25
	s_mov_b32 m0, s58
	s_nop 0
	global_load_lds_dwordx4 v148, s[48:49]
	s_mov_b32 m0, s59
	s_nop 0
	global_load_lds_dwordx4 v152, s[48:49]
	s_waitcnt vmcnt(8)
	s_waitcnt lgkmcnt(0)
	s_barrier
	s_setprio 1
	v_mfma_f32_16x16x128_f8f6f4 v[86:89], v[166:169], v[182:185], v[86:89] cbsz:4 blgp:4
	v_mfma_f32_16x16x128_f8f6f4 v[86:89], v[174:177], v[190:193], v[86:89] cbsz:4 blgp:4
	v_mfma_f32_16x16x128_f8f6f4 v[90:93], v[170:173], v[182:185], v[90:93] cbsz:4 blgp:4
	v_mfma_f32_16x16x128_f8f6f4 v[90:93], v[178:181], v[190:193], v[90:93] cbsz:4 blgp:4
	v_mfma_f32_16x16x128_f8f6f4 v[98:101], v[166:169], v[186:189], v[98:101] cbsz:4 blgp:4
	v_mfma_f32_16x16x128_f8f6f4 v[98:101], v[174:177], v[194:197], v[98:101] cbsz:4 blgp:4
	v_mfma_f32_16x16x128_f8f6f4 v[106:109], v[170:173], v[186:189], v[106:109] cbsz:4 blgp:4
	v_mfma_f32_16x16x128_f8f6f4 v[106:109], v[178:181], v[194:197], v[106:109] cbsz:4 blgp:4
	v_mfma_f32_16x16x128_f8f6f4 v[118:121], v[166:169], v[198:201], v[118:121] cbsz:4 blgp:4
	v_mfma_f32_16x16x128_f8f6f4 v[118:121], v[174:177], v[206:209], v[118:121] cbsz:4 blgp:4
	v_mfma_f32_16x16x128_f8f6f4 v[126:129], v[170:173], v[198:201], v[126:129] cbsz:4 blgp:4
	v_mfma_f32_16x16x128_f8f6f4 v[126:129], v[178:181], v[206:209], v[126:129] cbsz:4 blgp:4
	v_mfma_f32_16x16x128_f8f6f4 v[138:141], v[166:169], v[202:205], v[138:141] cbsz:4 blgp:4
	v_mfma_f32_16x16x128_f8f6f4 v[138:141], v[174:177], v[210:213], v[138:141] cbsz:4 blgp:4
	v_mfma_f32_16x16x128_f8f6f4 v[82:85], v[170:173], v[202:205], v[82:85] cbsz:4 blgp:4
	v_mfma_f32_16x16x128_f8f6f4 v[82:85], v[178:181], v[210:213], v[82:85] cbsz:4 blgp:4
	v_mfma_f32_16x16x128_f8f6f4 v[94:97], v[214:217], v[182:185], v[94:97] cbsz:4 blgp:4
	v_mfma_f32_16x16x128_f8f6f4 v[94:97], v[222:225], v[190:193], v[94:97] cbsz:4 blgp:4
	v_mfma_f32_16x16x128_f8f6f4 v[102:105], v[218:221], v[182:185], v[102:105] cbsz:4 blgp:4
	v_mfma_f32_16x16x128_f8f6f4 v[102:105], v[226:229], v[190:193], v[102:105] cbsz:4 blgp:4
	v_mfma_f32_16x16x128_f8f6f4 v[110:113], v[214:217], v[186:189], v[110:113] cbsz:4 blgp:4
	v_mfma_f32_16x16x128_f8f6f4 v[110:113], v[222:225], v[194:197], v[110:113] cbsz:4 blgp:4
	v_mfma_f32_16x16x128_f8f6f4 v[114:117], v[218:221], v[186:189], v[114:117] cbsz:4 blgp:4
	v_mfma_f32_16x16x128_f8f6f4 v[114:117], v[226:229], v[194:197], v[114:117] cbsz:4 blgp:4
	v_mfma_f32_16x16x128_f8f6f4 v[122:125], v[214:217], v[198:201], v[122:125] cbsz:4 blgp:4
	v_mfma_f32_16x16x128_f8f6f4 v[122:125], v[222:225], v[206:209], v[122:125] cbsz:4 blgp:4
	v_mfma_f32_16x16x128_f8f6f4 v[130:133], v[218:221], v[198:201], v[130:133] cbsz:4 blgp:4
	v_mfma_f32_16x16x128_f8f6f4 v[130:133], v[226:229], v[206:209], v[130:133] cbsz:4 blgp:4
	v_mfma_f32_16x16x128_f8f6f4 v[134:137], v[214:217], v[202:205], v[134:137] cbsz:4 blgp:4
	v_mfma_f32_16x16x128_f8f6f4 v[134:137], v[222:225], v[210:213], v[134:137] cbsz:4 blgp:4
	v_mfma_f32_16x16x128_f8f6f4 v[142:145], v[218:221], v[202:205], v[142:145] cbsz:4 blgp:4
	v_mfma_f32_16x16x128_f8f6f4 v[142:145], v[226:229], v[210:213], v[142:145] cbsz:4 blgp:4
	s_setprio 0
	s_barrier
	ds_read_b128 v[166:169], v161 offset:32768
	ds_read_b128 v[170:173], v161 offset:34816
	ds_read_b128 v[174:177], v162 offset:32768
	ds_read_b128 v[178:181], v162 offset:34816
	ds_read_b128 v[182:185], v163 offset:32768
	ds_read_b128 v[186:189], v163 offset:34816
	ds_read_b128 v[190:193], v164 offset:32768
	ds_read_b128 v[194:197], v164 offset:34816
	ds_read_b128 v[198:201], v163 offset:36864
	ds_read_b128 v[202:205], v163 offset:38912
	ds_read_b128 v[206:209], v164 offset:36864
	ds_read_b128 v[210:213], v164 offset:38912
	s_add_u32 s46, s46, s22
	s_addc_u32 s47, s47, s23
	s_mov_b32 m0, s60
	s_nop 0
	global_load_lds_dwordx4 v146, s[46:47]
	s_mov_b32 m0, s61
	s_nop 0
	global_load_lds_dwordx4 v150, s[46:47]
	s_waitcnt lgkmcnt(8)
	ds_read_b128 v[214:217], v161 offset:49152
	ds_read_b128 v[218:221], v161 offset:51200
	ds_read_b128 v[222:225], v162 offset:49152
	ds_read_b128 v[226:229], v162 offset:51200
	s_waitcnt vmcnt(8)
	s_waitcnt lgkmcnt(0)
	s_barrier
	s_waitcnt lgkmcnt(0)
	s_setprio 1
	v_mfma_f32_16x16x128_f8f6f4 v[18:21], v[166:169], v[182:185], v[18:21] cbsz:4 blgp:4
	v_mfma_f32_16x16x128_f8f6f4 v[18:21], v[174:177], v[190:193], v[18:21] cbsz:4 blgp:4
	v_mfma_f32_16x16x128_f8f6f4 v[22:25], v[170:173], v[182:185], v[22:25] cbsz:4 blgp:4
	v_mfma_f32_16x16x128_f8f6f4 v[22:25], v[178:181], v[190:193], v[22:25] cbsz:4 blgp:4
	v_mfma_f32_16x16x128_f8f6f4 v[26:29], v[166:169], v[186:189], v[26:29] cbsz:4 blgp:4
	v_mfma_f32_16x16x128_f8f6f4 v[26:29], v[174:177], v[194:197], v[26:29] cbsz:4 blgp:4
	v_mfma_f32_16x16x128_f8f6f4 v[30:33], v[170:173], v[186:189], v[30:33] cbsz:4 blgp:4
	v_mfma_f32_16x16x128_f8f6f4 v[30:33], v[178:181], v[194:197], v[30:33] cbsz:4 blgp:4
	v_mfma_f32_16x16x128_f8f6f4 v[34:37], v[166:169], v[198:201], v[34:37] cbsz:4 blgp:4
	v_mfma_f32_16x16x128_f8f6f4 v[34:37], v[174:177], v[206:209], v[34:37] cbsz:4 blgp:4
	v_mfma_f32_16x16x128_f8f6f4 v[38:41], v[170:173], v[198:201], v[38:41] cbsz:4 blgp:4
	v_mfma_f32_16x16x128_f8f6f4 v[38:41], v[178:181], v[206:209], v[38:41] cbsz:4 blgp:4
	v_mfma_f32_16x16x128_f8f6f4 v[42:45], v[166:169], v[202:205], v[42:45] cbsz:4 blgp:4
	v_mfma_f32_16x16x128_f8f6f4 v[42:45], v[174:177], v[210:213], v[42:45] cbsz:4 blgp:4
	v_mfma_f32_16x16x128_f8f6f4 v[46:49], v[170:173], v[202:205], v[46:49] cbsz:4 blgp:4
	v_mfma_f32_16x16x128_f8f6f4 v[46:49], v[178:181], v[210:213], v[46:49] cbsz:4 blgp:4
	v_mfma_f32_16x16x128_f8f6f4 v[50:53], v[214:217], v[182:185], v[50:53] cbsz:4 blgp:4
	v_mfma_f32_16x16x128_f8f6f4 v[50:53], v[222:225], v[190:193], v[50:53] cbsz:4 blgp:4
	v_mfma_f32_16x16x128_f8f6f4 v[54:57], v[218:221], v[182:185], v[54:57] cbsz:4 blgp:4
	v_mfma_f32_16x16x128_f8f6f4 v[54:57], v[226:229], v[190:193], v[54:57] cbsz:4 blgp:4
	v_mfma_f32_16x16x128_f8f6f4 v[58:61], v[214:217], v[186:189], v[58:61] cbsz:4 blgp:4
	v_mfma_f32_16x16x128_f8f6f4 v[58:61], v[222:225], v[194:197], v[58:61] cbsz:4 blgp:4
	v_mfma_f32_16x16x128_f8f6f4 v[62:65], v[218:221], v[186:189], v[62:65] cbsz:4 blgp:4
	v_mfma_f32_16x16x128_f8f6f4 v[62:65], v[226:229], v[194:197], v[62:65] cbsz:4 blgp:4
	v_mfma_f32_16x16x128_f8f6f4 v[66:69], v[214:217], v[198:201], v[66:69] cbsz:4 blgp:4
	v_mfma_f32_16x16x128_f8f6f4 v[66:69], v[222:225], v[206:209], v[66:69] cbsz:4 blgp:4
	v_mfma_f32_16x16x128_f8f6f4 v[70:73], v[218:221], v[198:201], v[70:73] cbsz:4 blgp:4
	v_mfma_f32_16x16x128_f8f6f4 v[70:73], v[226:229], v[206:209], v[70:73] cbsz:4 blgp:4
	v_mfma_f32_16x16x128_f8f6f4 v[74:77], v[214:217], v[202:205], v[74:77] cbsz:4 blgp:4
	v_mfma_f32_16x16x128_f8f6f4 v[74:77], v[222:225], v[210:213], v[74:77] cbsz:4 blgp:4
	v_mfma_f32_16x16x128_f8f6f4 v[78:81], v[218:221], v[202:205], v[78:81] cbsz:4 blgp:4
	v_mfma_f32_16x16x128_f8f6f4 v[78:81], v[226:229], v[210:213], v[78:81] cbsz:4 blgp:4
	s_setprio 0
	s_barrier
	s_mov_b32 m0, s64
	s_nop 0
	global_load_lds_dwordx4 v148, s[40:41]
	s_mov_b32 m0, s65
	s_nop 0
	global_load_lds_dwordx4 v152, s[40:41]
	ds_read_b128 v[182:185], v163 offset:49152
	ds_read_b128 v[186:189], v163 offset:51200
	ds_read_b128 v[190:193], v164 offset:49152
	ds_read_b128 v[194:197], v164 offset:51200
	ds_read_b128 v[198:201], v163 offset:53248
	ds_read_b128 v[202:205], v163 offset:55296
	ds_read_b128 v[206:209], v164 offset:53248
	ds_read_b128 v[210:213], v164 offset:55296
	s_mov_b32 m0, s66
	s_nop 0
	global_load_lds_dwordx4 v146, s[44:45]
	s_mov_b32 m0, s67
	s_nop 0
	global_load_lds_dwordx4 v150, s[44:45]
	s_add_u32 s40, s40, s24
	s_addc_u32 s41, s41, s25
	s_mov_b32 m0, s68
	s_nop 0
	global_load_lds_dwordx4 v148, s[40:41]
	s_mov_b32 m0, s69
	s_nop 0
	global_load_lds_dwordx4 v152, s[40:41]
	s_waitcnt vmcnt(8)
	s_waitcnt lgkmcnt(0)
	s_barrier
	s_setprio 1
	v_mfma_f32_16x16x128_f8f6f4 v[86:89], v[166:169], v[182:185], v[86:89] cbsz:4 blgp:4
	v_mfma_f32_16x16x128_f8f6f4 v[86:89], v[174:177], v[190:193], v[86:89] cbsz:4 blgp:4
	v_mfma_f32_16x16x128_f8f6f4 v[90:93], v[170:173], v[182:185], v[90:93] cbsz:4 blgp:4
	v_mfma_f32_16x16x128_f8f6f4 v[90:93], v[178:181], v[190:193], v[90:93] cbsz:4 blgp:4
	v_mfma_f32_16x16x128_f8f6f4 v[98:101], v[166:169], v[186:189], v[98:101] cbsz:4 blgp:4
	v_mfma_f32_16x16x128_f8f6f4 v[98:101], v[174:177], v[194:197], v[98:101] cbsz:4 blgp:4
	v_mfma_f32_16x16x128_f8f6f4 v[106:109], v[170:173], v[186:189], v[106:109] cbsz:4 blgp:4
	v_mfma_f32_16x16x128_f8f6f4 v[106:109], v[178:181], v[194:197], v[106:109] cbsz:4 blgp:4
	v_mfma_f32_16x16x128_f8f6f4 v[118:121], v[166:169], v[198:201], v[118:121] cbsz:4 blgp:4
	v_mfma_f32_16x16x128_f8f6f4 v[118:121], v[174:177], v[206:209], v[118:121] cbsz:4 blgp:4
	v_mfma_f32_16x16x128_f8f6f4 v[126:129], v[170:173], v[198:201], v[126:129] cbsz:4 blgp:4
	v_mfma_f32_16x16x128_f8f6f4 v[126:129], v[178:181], v[206:209], v[126:129] cbsz:4 blgp:4
	v_mfma_f32_16x16x128_f8f6f4 v[138:141], v[166:169], v[202:205], v[138:141] cbsz:4 blgp:4
	v_mfma_f32_16x16x128_f8f6f4 v[138:141], v[174:177], v[210:213], v[138:141] cbsz:4 blgp:4
	v_mfma_f32_16x16x128_f8f6f4 v[82:85], v[170:173], v[202:205], v[82:85] cbsz:4 blgp:4
	v_mfma_f32_16x16x128_f8f6f4 v[82:85], v[178:181], v[210:213], v[82:85] cbsz:4 blgp:4
	v_mfma_f32_16x16x128_f8f6f4 v[94:97], v[214:217], v[182:185], v[94:97] cbsz:4 blgp:4
	v_mfma_f32_16x16x128_f8f6f4 v[94:97], v[222:225], v[190:193], v[94:97] cbsz:4 blgp:4
	v_mfma_f32_16x16x128_f8f6f4 v[102:105], v[218:221], v[182:185], v[102:105] cbsz:4 blgp:4
	v_mfma_f32_16x16x128_f8f6f4 v[102:105], v[226:229], v[190:193], v[102:105] cbsz:4 blgp:4
	v_mfma_f32_16x16x128_f8f6f4 v[110:113], v[214:217], v[186:189], v[110:113] cbsz:4 blgp:4
	v_mfma_f32_16x16x128_f8f6f4 v[110:113], v[222:225], v[194:197], v[110:113] cbsz:4 blgp:4
	v_mfma_f32_16x16x128_f8f6f4 v[114:117], v[218:221], v[186:189], v[114:117] cbsz:4 blgp:4
	v_mfma_f32_16x16x128_f8f6f4 v[114:117], v[226:229], v[194:197], v[114:117] cbsz:4 blgp:4
	v_mfma_f32_16x16x128_f8f6f4 v[122:125], v[214:217], v[198:201], v[122:125] cbsz:4 blgp:4
	v_mfma_f32_16x16x128_f8f6f4 v[122:125], v[222:225], v[206:209], v[122:125] cbsz:4 blgp:4
	v_mfma_f32_16x16x128_f8f6f4 v[130:133], v[218:221], v[198:201], v[130:133] cbsz:4 blgp:4
	v_mfma_f32_16x16x128_f8f6f4 v[130:133], v[226:229], v[206:209], v[130:133] cbsz:4 blgp:4
	v_mfma_f32_16x16x128_f8f6f4 v[134:137], v[214:217], v[202:205], v[134:137] cbsz:4 blgp:4
	v_mfma_f32_16x16x128_f8f6f4 v[134:137], v[222:225], v[210:213], v[134:137] cbsz:4 blgp:4
	v_mfma_f32_16x16x128_f8f6f4 v[142:145], v[218:221], v[202:205], v[142:145] cbsz:4 blgp:4
	v_mfma_f32_16x16x128_f8f6f4 v[142:145], v[226:229], v[210:213], v[142:145] cbsz:4 blgp:4
	s_setprio 0
	s_add_i32 s40, s81, 2
	s_add_u32 s29, s29, 0x100
	s_addc_u32 s78, s78, 0
	s_add_u32 s79, s79, 0x100
	s_addc_u32 s80, s80, 0
	s_add_u32 s38, s38, 0x100
	s_addc_u32 s39, s39, 0
	s_cmp_ge_i32 s81, s63
	s_barrier
	s_cbranch_scc1 .LBB4_4
	s_mov_b32 s81, s40
	s_cmp_eq_u32 s63, s81
	s_cselect_b64 s[40:41], -1, 0
	s_cmp_lg_u32 s63, s81
	s_cbranch_scc0 .LBB4_14
	s_branch .LBB4_15

.Lrs_a_5:
	s_add_u32 s82, s42, s22
	s_addc_u32 s83, s43, s23
	s_add_u32 s29, s42, 0x100
	s_addc_u32 s46, s43, 0
	s_and_b64 s[44:45], s[14:15], exec
	ds_read_b128 v[82:85], v163
	ds_read_b128 v[94:97], v163 offset:2048
	ds_read_b128 v[102:105], v164
	ds_read_b128 v[110:113], v164 offset:2048
	s_cselect_b32 s49, s39, s46
	s_cselect_b32 s48, s38, s29
	s_add_u32 s29, s40, 0x100
	s_addc_u32 s46, s41, 0
	s_and_b64 s[44:45], s[14:15], exec
	s_cselect_b32 s51, s5, s46
	s_cselect_b32 s50, s4, s29
	s_add_u32 s46, s48, 0x80
	s_addc_u32 s47, s49, 0
	s_add_u32 s44, s50, 0x80
	s_addc_u32 s45, s51, 0
	ds_read_b128 v[58:61], v165
	ds_read_b128 v[66:69], v165 offset:2048
	ds_read_b128 v[62:65], v166
	ds_read_b128 v[70:73], v166 offset:2048
	ds_read_b128 v[74:77], v165 offset:4096
	ds_read_b128 v[86:89], v165 offset:6144
	ds_read_b128 v[78:81], v166 offset:4096
	ds_read_b128 v[90:93], v166 offset:6144
	s_add_u32 s80, s82, 0x80
	s_addc_u32 s81, s83, 0
	s_mov_b32 m0, s71
	s_nop 0
	global_load_lds_dwordx4 v146, s[80:81]
	s_mov_b32 m0, s72
	s_nop 0
	global_load_lds_dwordx4 v150, s[80:81]
	s_waitcnt lgkmcnt(8)
	ds_read_b128 v[142:145], v163 offset:16384
	ds_read_b128 v[156:159], v163 offset:18432
	ds_read_b128 v[168:171], v164 offset:16384
	ds_read_b128 v[172:175], v164 offset:18432
	s_waitcnt vmcnt(8)
	s_waitcnt lgkmcnt(0)
	s_barrier
	s_waitcnt lgkmcnt(0)
	s_waitcnt vmcnt(16)
	v_mov_b32_e32 v1, v0
	v_pk_mul_f32 v[16:17], v[0:1], v[16:17]
	v_pk_mul_f32 v[14:15], v[154:155], v[14:15]
	v_pk_mul_f32 v[12:13], v[0:1], v[12:13]
	v_pk_mul_f32 v[10:11], v[154:155], v[10:11]
	v_pk_mul_f32 v[8:9], v[0:1], v[8:9]
	v_pk_mul_f32 v[6:7], v[154:155], v[6:7]
	v_pk_mul_f32 v[4:5], v[0:1], v[4:5]
	v_pk_mul_f32 v[2:3], v[154:155], v[2:3]
	s_setprio 1
	v_mfma_f32_16x16x128_f8f6f4 v[18:21], v[82:85], v[58:61], v[14:17] cbsz:4 blgp:4
	v_mfma_f32_16x16x128_f8f6f4 v[18:21], v[102:105], v[62:65], v[18:21] cbsz:4 blgp:4
	v_mfma_f32_16x16x128_f8f6f4 v[22:25], v[94:97], v[58:61], v[10:13] cbsz:4 blgp:4
	v_mfma_f32_16x16x128_f8f6f4 v[22:25], v[110:113], v[62:65], v[22:25] cbsz:4 blgp:4
	v_mfma_f32_16x16x128_f8f6f4 v[26:29], v[82:85], v[66:69], v[14:17] cbsz:4 blgp:4
	v_mfma_f32_16x16x128_f8f6f4 v[26:29], v[102:105], v[70:73], v[26:29] cbsz:4 blgp:4
	v_mfma_f32_16x16x128_f8f6f4 v[30:33], v[94:97], v[66:69], v[10:13] cbsz:4 blgp:4
	v_mfma_f32_16x16x128_f8f6f4 v[30:33], v[110:113], v[70:73], v[30:33] cbsz:4 blgp:4
	v_mfma_f32_16x16x128_f8f6f4 v[34:37], v[82:85], v[74:77], v[14:17] cbsz:4 blgp:4
	v_mfma_f32_16x16x128_f8f6f4 v[34:37], v[102:105], v[78:81], v[34:37] cbsz:4 blgp:4
	v_mfma_f32_16x16x128_f8f6f4 v[38:41], v[94:97], v[74:77], v[10:13] cbsz:4 blgp:4
	v_mfma_f32_16x16x128_f8f6f4 v[38:41], v[110:113], v[78:81], v[38:41] cbsz:4 blgp:4
	v_mfma_f32_16x16x128_f8f6f4 v[42:45], v[82:85], v[86:89], v[14:17] cbsz:4 blgp:4
	v_mfma_f32_16x16x128_f8f6f4 v[42:45], v[102:105], v[90:93], v[42:45] cbsz:4 blgp:4
	v_mfma_f32_16x16x128_f8f6f4 v[46:49], v[94:97], v[86:89], v[10:13] cbsz:4 blgp:4
	v_mfma_f32_16x16x128_f8f6f4 v[46:49], v[110:113], v[90:93], v[46:49] cbsz:4 blgp:4
	v_mfma_f32_16x16x128_f8f6f4 v[50:53], v[142:145], v[58:61], v[6:9] cbsz:4 blgp:4
	v_mfma_f32_16x16x128_f8f6f4 v[50:53], v[168:171], v[62:65], v[50:53] cbsz:4 blgp:4
	v_mfma_f32_16x16x128_f8f6f4 v[54:57], v[156:159], v[58:61], v[2:5] cbsz:4 blgp:4
	v_mfma_f32_16x16x128_f8f6f4 v[54:57], v[172:175], v[62:65], v[54:57] cbsz:4 blgp:4
	v_mfma_f32_16x16x128_f8f6f4 v[58:61], v[142:145], v[66:69], v[6:9] cbsz:4 blgp:4
	v_mfma_f32_16x16x128_f8f6f4 v[58:61], v[168:171], v[70:73], v[58:61] cbsz:4 blgp:4
	v_mfma_f32_16x16x128_f8f6f4 v[62:65], v[156:159], v[66:69], v[2:5] cbsz:4 blgp:4
	v_mfma_f32_16x16x128_f8f6f4 v[62:65], v[172:175], v[70:73], v[62:65] cbsz:4 blgp:4
	v_mfma_f32_16x16x128_f8f6f4 v[66:69], v[142:145], v[74:77], v[6:9] cbsz:4 blgp:4
	v_mfma_f32_16x16x128_f8f6f4 v[66:69], v[168:171], v[78:81], v[66:69] cbsz:4 blgp:4
	v_mfma_f32_16x16x128_f8f6f4 v[70:73], v[156:159], v[74:77], v[2:5] cbsz:4 blgp:4
	v_mfma_f32_16x16x128_f8f6f4 v[70:73], v[172:175], v[78:81], v[70:73] cbsz:4 blgp:4
	v_mfma_f32_16x16x128_f8f6f4 v[74:77], v[142:145], v[86:89], v[6:9] cbsz:4 blgp:4
	v_mfma_f32_16x16x128_f8f6f4 v[74:77], v[168:171], v[90:93], v[74:77] cbsz:4 blgp:4
	v_mfma_f32_16x16x128_f8f6f4 v[78:81], v[156:159], v[86:89], v[2:5] cbsz:4 blgp:4
	v_mfma_f32_16x16x128_f8f6f4 v[78:81], v[172:175], v[90:93], v[78:81] cbsz:4 blgp:4
	s_setprio 0
	s_barrier
	s_mov_b32 m0, s56
	s_nop 0
	global_load_lds_dwordx4 v148, s[50:51]
	s_mov_b32 m0, s57
	s_nop 0
	global_load_lds_dwordx4 v152, s[50:51]
	ds_read_b128 v[114:117], v165 offset:16384
	ds_read_b128 v[122:125], v165 offset:18432
	ds_read_b128 v[130:133], v166 offset:16384
	ds_read_b128 v[134:137], v166 offset:18432
	ds_read_b128 v[176:179], v165 offset:20480
	ds_read_b128 v[180:183], v165 offset:22528
	ds_read_b128 v[184:187], v166 offset:20480
	ds_read_b128 v[188:191], v166 offset:22528
	s_mov_b32 m0, s55
	s_nop 0
	global_load_lds_dwordx4 v146, s[48:49]
	s_mov_b32 m0, s58
	s_nop 0
	global_load_lds_dwordx4 v150, s[48:49]
	s_add_u32 s50, s50, s24
	s_addc_u32 s51, s51, s25
	s_mov_b32 m0, s59
	s_nop 0
	global_load_lds_dwordx4 v148, s[50:51]
	s_mov_b32 m0, s60
	s_nop 0
	global_load_lds_dwordx4 v152, s[50:51]
	s_waitcnt vmcnt(8)
	s_waitcnt lgkmcnt(0)
	s_barrier
	s_setprio 1
	v_mfma_f32_16x16x128_f8f6f4 v[86:89], v[82:85], v[114:117], v[14:17] cbsz:4 blgp:4
	v_mfma_f32_16x16x128_f8f6f4 v[86:89], v[102:105], v[130:133], v[86:89] cbsz:4 blgp:4
	v_mfma_f32_16x16x128_f8f6f4 v[90:93], v[94:97], v[114:117], v[10:13] cbsz:4 blgp:4
	v_mfma_f32_16x16x128_f8f6f4 v[90:93], v[110:113], v[130:133], v[90:93] cbsz:4 blgp:4
	v_mfma_f32_16x16x128_f8f6f4 v[98:101], v[82:85], v[122:125], v[14:17] cbsz:4 blgp:4
	v_mfma_f32_16x16x128_f8f6f4 v[98:101], v[102:105], v[134:137], v[98:101] cbsz:4 blgp:4
	v_mfma_f32_16x16x128_f8f6f4 v[106:109], v[94:97], v[122:125], v[10:13] cbsz:4 blgp:4
	v_mfma_f32_16x16x128_f8f6f4 v[106:109], v[110:113], v[134:137], v[106:109] cbsz:4 blgp:4
	v_mfma_f32_16x16x128_f8f6f4 v[118:121], v[82:85], v[176:179], v[14:17] cbsz:4 blgp:4
	v_mfma_f32_16x16x128_f8f6f4 v[118:121], v[102:105], v[184:187], v[118:121] cbsz:4 blgp:4
	v_mfma_f32_16x16x128_f8f6f4 v[126:129], v[94:97], v[176:179], v[10:13] cbsz:4 blgp:4
	v_mfma_f32_16x16x128_f8f6f4 v[126:129], v[110:113], v[184:187], v[126:129] cbsz:4 blgp:4
	v_mfma_f32_16x16x128_f8f6f4 v[138:141], v[82:85], v[180:183], v[14:17] cbsz:4 blgp:4
	v_mfma_f32_16x16x128_f8f6f4 v[138:141], v[102:105], v[188:191], v[138:141] cbsz:4 blgp:4
	v_mfma_f32_16x16x128_f8f6f4 v[82:85], v[94:97], v[180:183], v[10:13] cbsz:4 blgp:4
	v_mfma_f32_16x16x128_f8f6f4 v[82:85], v[110:113], v[188:191], v[82:85] cbsz:4 blgp:4
	v_mfma_f32_16x16x128_f8f6f4 v[94:97], v[142:145], v[114:117], v[6:9] cbsz:4 blgp:4
	v_mfma_f32_16x16x128_f8f6f4 v[94:97], v[168:171], v[130:133], v[94:97] cbsz:4 blgp:4
	v_mfma_f32_16x16x128_f8f6f4 v[102:105], v[156:159], v[114:117], v[2:5] cbsz:4 blgp:4
	v_mfma_f32_16x16x128_f8f6f4 v[102:105], v[172:175], v[130:133], v[102:105] cbsz:4 blgp:4
	v_mfma_f32_16x16x128_f8f6f4 v[110:113], v[142:145], v[122:125], v[6:9] cbsz:4 blgp:4
	v_mfma_f32_16x16x128_f8f6f4 v[110:113], v[168:171], v[134:137], v[110:113] cbsz:4 blgp:4
	v_mfma_f32_16x16x128_f8f6f4 v[114:117], v[156:159], v[122:125], v[2:5] cbsz:4 blgp:4
	v_mfma_f32_16x16x128_f8f6f4 v[114:117], v[172:175], v[134:137], v[114:117] cbsz:4 blgp:4
	v_mfma_f32_16x16x128_f8f6f4 v[122:125], v[142:145], v[176:179], v[6:9] cbsz:4 blgp:4
	v_mfma_f32_16x16x128_f8f6f4 v[122:125], v[168:171], v[184:187], v[122:125] cbsz:4 blgp:4
	v_mfma_f32_16x16x128_f8f6f4 v[130:133], v[156:159], v[176:179], v[2:5] cbsz:4 blgp:4
	v_mfma_f32_16x16x128_f8f6f4 v[130:133], v[172:175], v[184:187], v[130:133] cbsz:4 blgp:4
	v_mfma_f32_16x16x128_f8f6f4 v[134:137], v[142:145], v[180:183], v[6:9] cbsz:4 blgp:4
	v_mfma_f32_16x16x128_f8f6f4 v[134:137], v[168:171], v[188:191], v[134:137] cbsz:4 blgp:4
	v_mfma_f32_16x16x128_f8f6f4 v[142:145], v[156:159], v[180:183], v[2:5] cbsz:4 blgp:4
	v_mfma_f32_16x16x128_f8f6f4 v[142:145], v[172:175], v[188:191], v[142:145] cbsz:4 blgp:4
	s_setprio 0
	s_barrier
	ds_read_b128 v[156:159], v163 offset:32768
	ds_read_b128 v[168:171], v163 offset:34816
	ds_read_b128 v[172:175], v164 offset:32768
	ds_read_b128 v[176:179], v164 offset:34816
	ds_read_b128 v[180:183], v165 offset:32768
	ds_read_b128 v[184:187], v165 offset:34816
	ds_read_b128 v[188:191], v166 offset:32768
	ds_read_b128 v[192:195], v166 offset:34816
	ds_read_b128 v[196:199], v165 offset:36864
	ds_read_b128 v[200:203], v165 offset:38912
	ds_read_b128 v[204:207], v166 offset:36864
	ds_read_b128 v[208:211], v166 offset:38912
	s_add_u32 s48, s48, s22
	s_addc_u32 s49, s49, s23
	s_mov_b32 m0, s61
	s_nop 0
	global_load_lds_dwordx4 v146, s[48:49]
	s_mov_b32 m0, s62
	s_nop 0
	global_load_lds_dwordx4 v150, s[48:49]
	s_waitcnt lgkmcnt(8)
	ds_read_b128 v[212:215], v163 offset:49152
	ds_read_b128 v[216:219], v163 offset:51200
	ds_read_b128 v[220:223], v164 offset:49152
	ds_read_b128 v[224:227], v164 offset:51200
	s_waitcnt vmcnt(8)
	s_waitcnt lgkmcnt(0)
	s_barrier
	s_waitcnt lgkmcnt(0)
	s_setprio 1
	v_mfma_f32_16x16x128_f8f6f4 v[18:21], v[156:159], v[180:183], v[18:21] cbsz:4 blgp:4
	v_mfma_f32_16x16x128_f8f6f4 v[18:21], v[172:175], v[188:191], v[18:21] cbsz:4 blgp:4
	v_mfma_f32_16x16x128_f8f6f4 v[22:25], v[168:171], v[180:183], v[22:25] cbsz:4 blgp:4
	v_mfma_f32_16x16x128_f8f6f4 v[22:25], v[176:179], v[188:191], v[22:25] cbsz:4 blgp:4
	v_mfma_f32_16x16x128_f8f6f4 v[26:29], v[156:159], v[184:187], v[26:29] cbsz:4 blgp:4
	v_mfma_f32_16x16x128_f8f6f4 v[26:29], v[172:175], v[192:195], v[26:29] cbsz:4 blgp:4
	v_mfma_f32_16x16x128_f8f6f4 v[30:33], v[168:171], v[184:187], v[30:33] cbsz:4 blgp:4
	v_mfma_f32_16x16x128_f8f6f4 v[30:33], v[176:179], v[192:195], v[30:33] cbsz:4 blgp:4
	v_mfma_f32_16x16x128_f8f6f4 v[34:37], v[156:159], v[196:199], v[34:37] cbsz:4 blgp:4
	v_mfma_f32_16x16x128_f8f6f4 v[34:37], v[172:175], v[204:207], v[34:37] cbsz:4 blgp:4
	v_mfma_f32_16x16x128_f8f6f4 v[38:41], v[168:171], v[196:199], v[38:41] cbsz:4 blgp:4
	v_mfma_f32_16x16x128_f8f6f4 v[38:41], v[176:179], v[204:207], v[38:41] cbsz:4 blgp:4
	v_mfma_f32_16x16x128_f8f6f4 v[42:45], v[156:159], v[200:203], v[42:45] cbsz:4 blgp:4
	v_mfma_f32_16x16x128_f8f6f4 v[42:45], v[172:175], v[208:211], v[42:45] cbsz:4 blgp:4
	v_mfma_f32_16x16x128_f8f6f4 v[46:49], v[168:171], v[200:203], v[46:49] cbsz:4 blgp:4
	v_mfma_f32_16x16x128_f8f6f4 v[46:49], v[176:179], v[208:211], v[46:49] cbsz:4 blgp:4
	v_mfma_f32_16x16x128_f8f6f4 v[50:53], v[212:215], v[180:183], v[50:53] cbsz:4 blgp:4
	v_mfma_f32_16x16x128_f8f6f4 v[50:53], v[220:223], v[188:191], v[50:53] cbsz:4 blgp:4
	v_mfma_f32_16x16x128_f8f6f4 v[54:57], v[216:219], v[180:183], v[54:57] cbsz:4 blgp:4
	v_mfma_f32_16x16x128_f8f6f4 v[54:57], v[224:227], v[188:191], v[54:57] cbsz:4 blgp:4
	v_mfma_f32_16x16x128_f8f6f4 v[58:61], v[212:215], v[184:187], v[58:61] cbsz:4 blgp:4
	v_mfma_f32_16x16x128_f8f6f4 v[58:61], v[220:223], v[192:195], v[58:61] cbsz:4 blgp:4
	v_mfma_f32_16x16x128_f8f6f4 v[62:65], v[216:219], v[184:187], v[62:65] cbsz:4 blgp:4
	v_mfma_f32_16x16x128_f8f6f4 v[62:65], v[224:227], v[192:195], v[62:65] cbsz:4 blgp:4
	v_mfma_f32_16x16x128_f8f6f4 v[66:69], v[212:215], v[196:199], v[66:69] cbsz:4 blgp:4
	v_mfma_f32_16x16x128_f8f6f4 v[66:69], v[220:223], v[204:207], v[66:69] cbsz:4 blgp:4
	v_mfma_f32_16x16x128_f8f6f4 v[70:73], v[216:219], v[196:199], v[70:73] cbsz:4 blgp:4
	v_mfma_f32_16x16x128_f8f6f4 v[70:73], v[224:227], v[204:207], v[70:73] cbsz:4 blgp:4
	v_mfma_f32_16x16x128_f8f6f4 v[74:77], v[212:215], v[200:203], v[74:77] cbsz:4 blgp:4
	v_mfma_f32_16x16x128_f8f6f4 v[74:77], v[220:223], v[208:211], v[74:77] cbsz:4 blgp:4
	v_mfma_f32_16x16x128_f8f6f4 v[78:81], v[216:219], v[200:203], v[78:81] cbsz:4 blgp:4
	v_mfma_f32_16x16x128_f8f6f4 v[78:81], v[224:227], v[208:211], v[78:81] cbsz:4 blgp:4
	s_setprio 0
	s_barrier
	s_mov_b32 m0, s65
	s_nop 0
	global_load_lds_dwordx4 v148, s[44:45]
	s_mov_b32 m0, s66
	s_nop 0
	global_load_lds_dwordx4 v152, s[44:45]
	ds_read_b128 v[180:183], v165 offset:49152
	ds_read_b128 v[184:187], v165 offset:51200
	ds_read_b128 v[188:191], v166 offset:49152
	ds_read_b128 v[192:195], v166 offset:51200
	ds_read_b128 v[196:199], v165 offset:53248
	ds_read_b128 v[200:203], v165 offset:55296
	ds_read_b128 v[204:207], v166 offset:53248
	ds_read_b128 v[208:211], v166 offset:55296
	s_mov_b32 m0, s67
	s_nop 0
	global_load_lds_dwordx4 v146, s[46:47]
	s_mov_b32 m0, s68
	s_nop 0
	global_load_lds_dwordx4 v150, s[46:47]
	s_add_u32 s44, s44, s24
	s_addc_u32 s45, s45, s25
	s_mov_b32 m0, s69
	s_nop 0
	global_load_lds_dwordx4 v148, s[44:45]
	s_mov_b32 m0, s70
	s_nop 0
	global_load_lds_dwordx4 v152, s[44:45]
	s_waitcnt vmcnt(8)
	s_waitcnt lgkmcnt(0)
	s_barrier
	s_setprio 1
	v_mfma_f32_16x16x128_f8f6f4 v[86:89], v[156:159], v[180:183], v[86:89] cbsz:4 blgp:4
	v_mfma_f32_16x16x128_f8f6f4 v[86:89], v[172:175], v[188:191], v[86:89] cbsz:4 blgp:4
	v_mfma_f32_16x16x128_f8f6f4 v[90:93], v[168:171], v[180:183], v[90:93] cbsz:4 blgp:4
	v_mfma_f32_16x16x128_f8f6f4 v[90:93], v[176:179], v[188:191], v[90:93] cbsz:4 blgp:4
	v_mfma_f32_16x16x128_f8f6f4 v[98:101], v[156:159], v[184:187], v[98:101] cbsz:4 blgp:4
	v_mfma_f32_16x16x128_f8f6f4 v[98:101], v[172:175], v[192:195], v[98:101] cbsz:4 blgp:4
	v_mfma_f32_16x16x128_f8f6f4 v[106:109], v[168:171], v[184:187], v[106:109] cbsz:4 blgp:4
	v_mfma_f32_16x16x128_f8f6f4 v[106:109], v[176:179], v[192:195], v[106:109] cbsz:4 blgp:4
	v_mfma_f32_16x16x128_f8f6f4 v[118:121], v[156:159], v[196:199], v[118:121] cbsz:4 blgp:4
	v_mfma_f32_16x16x128_f8f6f4 v[118:121], v[172:175], v[204:207], v[118:121] cbsz:4 blgp:4
	v_mfma_f32_16x16x128_f8f6f4 v[126:129], v[168:171], v[196:199], v[126:129] cbsz:4 blgp:4
	v_mfma_f32_16x16x128_f8f6f4 v[126:129], v[176:179], v[204:207], v[126:129] cbsz:4 blgp:4
	v_mfma_f32_16x16x128_f8f6f4 v[138:141], v[156:159], v[200:203], v[138:141] cbsz:4 blgp:4
	v_mfma_f32_16x16x128_f8f6f4 v[138:141], v[172:175], v[208:211], v[138:141] cbsz:4 blgp:4
	v_mfma_f32_16x16x128_f8f6f4 v[82:85], v[168:171], v[200:203], v[82:85] cbsz:4 blgp:4
	v_mfma_f32_16x16x128_f8f6f4 v[82:85], v[176:179], v[208:211], v[82:85] cbsz:4 blgp:4
	v_mfma_f32_16x16x128_f8f6f4 v[94:97], v[212:215], v[180:183], v[94:97] cbsz:4 blgp:4
	v_mfma_f32_16x16x128_f8f6f4 v[94:97], v[220:223], v[188:191], v[94:97] cbsz:4 blgp:4
	v_mfma_f32_16x16x128_f8f6f4 v[102:105], v[216:219], v[180:183], v[102:105] cbsz:4 blgp:4
	v_mfma_f32_16x16x128_f8f6f4 v[102:105], v[224:227], v[188:191], v[102:105] cbsz:4 blgp:4
	v_mfma_f32_16x16x128_f8f6f4 v[110:113], v[212:215], v[184:187], v[110:113] cbsz:4 blgp:4
	v_mfma_f32_16x16x128_f8f6f4 v[110:113], v[220:223], v[192:195], v[110:113] cbsz:4 blgp:4
	v_mfma_f32_16x16x128_f8f6f4 v[114:117], v[216:219], v[184:187], v[114:117] cbsz:4 blgp:4
	v_mfma_f32_16x16x128_f8f6f4 v[114:117], v[224:227], v[192:195], v[114:117] cbsz:4 blgp:4
	v_mfma_f32_16x16x128_f8f6f4 v[122:125], v[212:215], v[196:199], v[122:125] cbsz:4 blgp:4
	v_mfma_f32_16x16x128_f8f6f4 v[122:125], v[220:223], v[204:207], v[122:125] cbsz:4 blgp:4
	v_mfma_f32_16x16x128_f8f6f4 v[130:133], v[216:219], v[196:199], v[130:133] cbsz:4 blgp:4
	v_mfma_f32_16x16x128_f8f6f4 v[130:133], v[224:227], v[204:207], v[130:133] cbsz:4 blgp:4
	v_mfma_f32_16x16x128_f8f6f4 v[134:137], v[212:215], v[200:203], v[134:137] cbsz:4 blgp:4
	v_mfma_f32_16x16x128_f8f6f4 v[134:137], v[220:223], v[208:211], v[134:137] cbsz:4 blgp:4
	v_mfma_f32_16x16x128_f8f6f4 v[142:145], v[216:219], v[200:203], v[142:145] cbsz:4 blgp:4
	v_mfma_f32_16x16x128_f8f6f4 v[142:145], v[224:227], v[208:211], v[142:145] cbsz:4 blgp:4
	s_setprio 0
	s_andn2_b64 vcc, exec, s[34:35]
	s_barrier
	s_cbranch_vccnz .LBB5_4
	s_ashr_i32 s29, s28, 31
	s_lshl_b64 s[44:45], s[28:29], 10
	s_add_u32 s44, s10, s44
	s_addc_u32 s45, s11, s45
	s_add_u32 s29, s42, 0x200
	s_addc_u32 s79, s43, 0
	s_add_u32 s80, s40, 0x200
	s_addc_u32 s81, s41, 0
	s_add_u32 s40, s82, 0x180
	s_addc_u32 s41, s83, 0
	s_mov_b32 s82, 4
	s_cmp_eq_u32 s64, s82
	s_cselect_b64 s[42:43], -1, 0
	s_cmp_lg_u32 s64, s82
	s_cbranch_scc1 .LBB5_15

.LBB5_15:
	ds_read_b128 v[156:159], v163
	ds_read_b128 v[168:171], v163 offset:2048
	ds_read_b128 v[172:175], v164
	ds_read_b128 v[176:179], v164 offset:2048
	s_and_b64 s[42:43], s[42:43], exec
	s_cselect_b32 s48, s38, s29
	s_cselect_b32 s49, s39, s79
	s_cselect_b32 s51, s5, s81
	s_cselect_b32 s50, s4, s80
	s_add_u32 s46, s48, 0x80
	s_addc_u32 s47, s49, 0
	s_add_u32 s42, s50, 0x80
	s_addc_u32 s43, s51, 0
	ds_read_b128 v[180:183], v165
	ds_read_b128 v[184:187], v165 offset:2048
	ds_read_b128 v[188:191], v166
	ds_read_b128 v[192:195], v166 offset:2048
	ds_read_b128 v[196:199], v165 offset:4096
	ds_read_b128 v[200:203], v165 offset:6144
	ds_read_b128 v[204:207], v166 offset:4096
	ds_read_b128 v[208:211], v166 offset:6144
	s_mov_b32 m0, s71
	s_nop 0
	global_load_lds_dwordx4 v146, s[40:41]
	s_mov_b32 m0, s72
	s_nop 0
	global_load_lds_dwordx4 v150, s[40:41]
	s_waitcnt lgkmcnt(8)
	ds_read_b128 v[212:215], v163 offset:16384
	ds_read_b128 v[216:219], v163 offset:18432
	ds_read_b128 v[220:223], v164 offset:16384
	ds_read_b128 v[224:227], v164 offset:18432
	s_waitcnt vmcnt(8)
	s_waitcnt lgkmcnt(0)
	s_barrier
	s_waitcnt lgkmcnt(0)
	s_setprio 1
	v_mfma_f32_16x16x128_f8f6f4 v[18:21], v[156:159], v[180:183], v[18:21] cbsz:4 blgp:4
	v_mfma_f32_16x16x128_f8f6f4 v[18:21], v[172:175], v[188:191], v[18:21] cbsz:4 blgp:4
	v_mfma_f32_16x16x128_f8f6f4 v[22:25], v[168:171], v[180:183], v[22:25] cbsz:4 blgp:4
	v_mfma_f32_16x16x128_f8f6f4 v[22:25], v[176:179], v[188:191], v[22:25] cbsz:4 blgp:4
	v_mfma_f32_16x16x128_f8f6f4 v[26:29], v[156:159], v[184:187], v[26:29] cbsz:4 blgp:4
	v_mfma_f32_16x16x128_f8f6f4 v[26:29], v[172:175], v[192:195], v[26:29] cbsz:4 blgp:4
	v_mfma_f32_16x16x128_f8f6f4 v[30:33], v[168:171], v[184:187], v[30:33] cbsz:4 blgp:4
	v_mfma_f32_16x16x128_f8f6f4 v[30:33], v[176:179], v[192:195], v[30:33] cbsz:4 blgp:4
	v_mfma_f32_16x16x128_f8f6f4 v[34:37], v[156:159], v[196:199], v[34:37] cbsz:4 blgp:4
	v_mfma_f32_16x16x128_f8f6f4 v[34:37], v[172:175], v[204:207], v[34:37] cbsz:4 blgp:4
	v_mfma_f32_16x16x128_f8f6f4 v[38:41], v[168:171], v[196:199], v[38:41] cbsz:4 blgp:4
	v_mfma_f32_16x16x128_f8f6f4 v[38:41], v[176:179], v[204:207], v[38:41] cbsz:4 blgp:4
	v_mfma_f32_16x16x128_f8f6f4 v[42:45], v[156:159], v[200:203], v[42:45] cbsz:4 blgp:4
	v_mfma_f32_16x16x128_f8f6f4 v[42:45], v[172:175], v[208:211], v[42:45] cbsz:4 blgp:4
	v_mfma_f32_16x16x128_f8f6f4 v[46:49], v[168:171], v[200:203], v[46:49] cbsz:4 blgp:4
	v_mfma_f32_16x16x128_f8f6f4 v[46:49], v[176:179], v[208:211], v[46:49] cbsz:4 blgp:4
	v_mfma_f32_16x16x128_f8f6f4 v[50:53], v[212:215], v[180:183], v[50:53] cbsz:4 blgp:4
	v_mfma_f32_16x16x128_f8f6f4 v[50:53], v[220:223], v[188:191], v[50:53] cbsz:4 blgp:4
	v_mfma_f32_16x16x128_f8f6f4 v[54:57], v[216:219], v[180:183], v[54:57] cbsz:4 blgp:4
	v_mfma_f32_16x16x128_f8f6f4 v[54:57], v[224:227], v[188:191], v[54:57] cbsz:4 blgp:4
	v_mfma_f32_16x16x128_f8f6f4 v[58:61], v[212:215], v[184:187], v[58:61] cbsz:4 blgp:4
	v_mfma_f32_16x16x128_f8f6f4 v[58:61], v[220:223], v[192:195], v[58:61] cbsz:4 blgp:4
	v_mfma_f32_16x16x128_f8f6f4 v[62:65], v[216:219], v[184:187], v[62:65] cbsz:4 blgp:4
	v_mfma_f32_16x16x128_f8f6f4 v[62:65], v[224:227], v[192:195], v[62:65] cbsz:4 blgp:4
	v_mfma_f32_16x16x128_f8f6f4 v[66:69], v[212:215], v[196:199], v[66:69] cbsz:4 blgp:4
	v_mfma_f32_16x16x128_f8f6f4 v[66:69], v[220:223], v[204:207], v[66:69] cbsz:4 blgp:4
	v_mfma_f32_16x16x128_f8f6f4 v[70:73], v[216:219], v[196:199], v[70:73] cbsz:4 blgp:4
	v_mfma_f32_16x16x128_f8f6f4 v[70:73], v[224:227], v[204:207], v[70:73] cbsz:4 blgp:4
	v_mfma_f32_16x16x128_f8f6f4 v[74:77], v[212:215], v[200:203], v[74:77] cbsz:4 blgp:4
	v_mfma_f32_16x16x128_f8f6f4 v[74:77], v[220:223], v[208:211], v[74:77] cbsz:4 blgp:4
	v_mfma_f32_16x16x128_f8f6f4 v[78:81], v[216:219], v[200:203], v[78:81] cbsz:4 blgp:4
	v_mfma_f32_16x16x128_f8f6f4 v[78:81], v[224:227], v[208:211], v[78:81] cbsz:4 blgp:4
	s_setprio 0
	s_barrier
	s_mov_b32 m0, s56
	s_nop 0
	global_load_lds_dwordx4 v148, s[50:51]
	s_mov_b32 m0, s57
	s_nop 0
	global_load_lds_dwordx4 v152, s[50:51]
	ds_read_b128 v[180:183], v165 offset:16384
	ds_read_b128 v[184:187], v165 offset:18432
	ds_read_b128 v[188:191], v166 offset:16384
	ds_read_b128 v[192:195], v166 offset:18432
	ds_read_b128 v[196:199], v165 offset:20480
	ds_read_b128 v[200:203], v165 offset:22528
	ds_read_b128 v[204:207], v166 offset:20480
	ds_read_b128 v[208:211], v166 offset:22528
	s_mov_b32 m0, s55
	s_nop 0
	global_load_lds_dwordx4 v146, s[48:49]
	s_mov_b32 m0, s58
	s_nop 0
	global_load_lds_dwordx4 v150, s[48:49]
	s_add_u32 s50, s50, s24
	s_addc_u32 s51, s51, s25
	s_mov_b32 m0, s59
	s_nop 0
	global_load_lds_dwordx4 v148, s[50:51]
	s_mov_b32 m0, s60
	s_nop 0
	global_load_lds_dwordx4 v152, s[50:51]
	s_waitcnt vmcnt(8)
	s_waitcnt lgkmcnt(0)
	s_barrier
	s_setprio 1
	v_mfma_f32_16x16x128_f8f6f4 v[86:89], v[156:159], v[180:183], v[86:89] cbsz:4 blgp:4
	v_mfma_f32_16x16x128_f8f6f4 v[86:89], v[172:175], v[188:191], v[86:89] cbsz:4 blgp:4
	v_mfma_f32_16x16x128_f8f6f4 v[90:93], v[168:171], v[180:183], v[90:93] cbsz:4 blgp:4
	v_mfma_f32_16x16x128_f8f6f4 v[90:93], v[176:179], v[188:191], v[90:93] cbsz:4 blgp:4
	v_mfma_f32_16x16x128_f8f6f4 v[98:101], v[156:159], v[184:187], v[98:101] cbsz:4 blgp:4
	v_mfma_f32_16x16x128_f8f6f4 v[98:101], v[172:175], v[192:195], v[98:101] cbsz:4 blgp:4
	v_mfma_f32_16x16x128_f8f6f4 v[106:109], v[168:171], v[184:187], v[106:109] cbsz:4 blgp:4
	v_mfma_f32_16x16x128_f8f6f4 v[106:109], v[176:179], v[192:195], v[106:109] cbsz:4 blgp:4
	v_mfma_f32_16x16x128_f8f6f4 v[118:121], v[156:159], v[196:199], v[118:121] cbsz:4 blgp:4
	v_mfma_f32_16x16x128_f8f6f4 v[118:121], v[172:175], v[204:207], v[118:121] cbsz:4 blgp:4
	v_mfma_f32_16x16x128_f8f6f4 v[126:129], v[168:171], v[196:199], v[126:129] cbsz:4 blgp:4
	v_mfma_f32_16x16x128_f8f6f4 v[126:129], v[176:179], v[204:207], v[126:129] cbsz:4 blgp:4
	v_mfma_f32_16x16x128_f8f6f4 v[138:141], v[156:159], v[200:203], v[138:141] cbsz:4 blgp:4
	v_mfma_f32_16x16x128_f8f6f4 v[138:141], v[172:175], v[208:211], v[138:141] cbsz:4 blgp:4
	v_mfma_f32_16x16x128_f8f6f4 v[82:85], v[168:171], v[200:203], v[82:85] cbsz:4 blgp:4
	v_mfma_f32_16x16x128_f8f6f4 v[82:85], v[176:179], v[208:211], v[82:85] cbsz:4 blgp:4
	v_mfma_f32_16x16x128_f8f6f4 v[94:97], v[212:215], v[180:183], v[94:97] cbsz:4 blgp:4
	v_mfma_f32_16x16x128_f8f6f4 v[94:97], v[220:223], v[188:191], v[94:97] cbsz:4 blgp:4
	v_mfma_f32_16x16x128_f8f6f4 v[102:105], v[216:219], v[180:183], v[102:105] cbsz:4 blgp:4
	v_mfma_f32_16x16x128_f8f6f4 v[102:105], v[224:227], v[188:191], v[102:105] cbsz:4 blgp:4
	v_mfma_f32_16x16x128_f8f6f4 v[110:113], v[212:215], v[184:187], v[110:113] cbsz:4 blgp:4
	v_mfma_f32_16x16x128_f8f6f4 v[110:113], v[220:223], v[192:195], v[110:113] cbsz:4 blgp:4
	v_mfma_f32_16x16x128_f8f6f4 v[114:117], v[216:219], v[184:187], v[114:117] cbsz:4 blgp:4
	v_mfma_f32_16x16x128_f8f6f4 v[114:117], v[224:227], v[192:195], v[114:117] cbsz:4 blgp:4
	v_mfma_f32_16x16x128_f8f6f4 v[122:125], v[212:215], v[196:199], v[122:125] cbsz:4 blgp:4
	v_mfma_f32_16x16x128_f8f6f4 v[122:125], v[220:223], v[204:207], v[122:125] cbsz:4 blgp:4
	v_mfma_f32_16x16x128_f8f6f4 v[130:133], v[216:219], v[196:199], v[130:133] cbsz:4 blgp:4
	v_mfma_f32_16x16x128_f8f6f4 v[130:133], v[224:227], v[204:207], v[130:133] cbsz:4 blgp:4
	v_mfma_f32_16x16x128_f8f6f4 v[134:137], v[212:215], v[200:203], v[134:137] cbsz:4 blgp:4
	v_mfma_f32_16x16x128_f8f6f4 v[134:137], v[220:223], v[208:211], v[134:137] cbsz:4 blgp:4
	v_mfma_f32_16x16x128_f8f6f4 v[142:145], v[216:219], v[200:203], v[142:145] cbsz:4 blgp:4
	v_mfma_f32_16x16x128_f8f6f4 v[142:145], v[224:227], v[208:211], v[142:145] cbsz:4 blgp:4
	s_setprio 0
	s_barrier
	ds_read_b128 v[156:159], v163 offset:32768
	ds_read_b128 v[168:171], v163 offset:34816
	ds_read_b128 v[172:175], v164 offset:32768
	ds_read_b128 v[176:179], v164 offset:34816
	ds_read_b128 v[180:183], v165 offset:32768
	ds_read_b128 v[184:187], v165 offset:34816
	ds_read_b128 v[188:191], v166 offset:32768
	ds_read_b128 v[192:195], v166 offset:34816
	ds_read_b128 v[196:199], v165 offset:36864
	ds_read_b128 v[200:203], v165 offset:38912
	ds_read_b128 v[204:207], v166 offset:36864
	ds_read_b128 v[208:211], v166 offset:38912
	s_add_u32 s48, s48, s22
	s_addc_u32 s49, s49, s23
	s_mov_b32 m0, s61
	s_nop 0
	global_load_lds_dwordx4 v146, s[48:49]
	s_mov_b32 m0, s62
	s_nop 0
	global_load_lds_dwordx4 v150, s[48:49]
	s_waitcnt lgkmcnt(8)
	ds_read_b128 v[212:215], v163 offset:49152
	ds_read_b128 v[216:219], v163 offset:51200
	ds_read_b128 v[220:223], v164 offset:49152
	ds_read_b128 v[224:227], v164 offset:51200
	s_waitcnt vmcnt(8)
	s_waitcnt lgkmcnt(0)
	s_barrier
	s_waitcnt lgkmcnt(0)
	s_setprio 1
	v_mfma_f32_16x16x128_f8f6f4 v[18:21], v[156:159], v[180:183], v[18:21] cbsz:4 blgp:4
	v_mfma_f32_16x16x128_f8f6f4 v[18:21], v[172:175], v[188:191], v[18:21] cbsz:4 blgp:4
	v_mfma_f32_16x16x128_f8f6f4 v[22:25], v[168:171], v[180:183], v[22:25] cbsz:4 blgp:4
	v_mfma_f32_16x16x128_f8f6f4 v[22:25], v[176:179], v[188:191], v[22:25] cbsz:4 blgp:4
	v_mfma_f32_16x16x128_f8f6f4 v[26:29], v[156:159], v[184:187], v[26:29] cbsz:4 blgp:4
	v_mfma_f32_16x16x128_f8f6f4 v[26:29], v[172:175], v[192:195], v[26:29] cbsz:4 blgp:4
	v_mfma_f32_16x16x128_f8f6f4 v[30:33], v[168:171], v[184:187], v[30:33] cbsz:4 blgp:4
	v_mfma_f32_16x16x128_f8f6f4 v[30:33], v[176:179], v[192:195], v[30:33] cbsz:4 blgp:4
	v_mfma_f32_16x16x128_f8f6f4 v[34:37], v[156:159], v[196:199], v[34:37] cbsz:4 blgp:4
	v_mfma_f32_16x16x128_f8f6f4 v[34:37], v[172:175], v[204:207], v[34:37] cbsz:4 blgp:4
	v_mfma_f32_16x16x128_f8f6f4 v[38:41], v[168:171], v[196:199], v[38:41] cbsz:4 blgp:4
	v_mfma_f32_16x16x128_f8f6f4 v[38:41], v[176:179], v[204:207], v[38:41] cbsz:4 blgp:4
	v_mfma_f32_16x16x128_f8f6f4 v[42:45], v[156:159], v[200:203], v[42:45] cbsz:4 blgp:4
	v_mfma_f32_16x16x128_f8f6f4 v[42:45], v[172:175], v[208:211], v[42:45] cbsz:4 blgp:4
	v_mfma_f32_16x16x128_f8f6f4 v[46:49], v[168:171], v[200:203], v[46:49] cbsz:4 blgp:4
	v_mfma_f32_16x16x128_f8f6f4 v[46:49], v[176:179], v[208:211], v[46:49] cbsz:4 blgp:4
	v_mfma_f32_16x16x128_f8f6f4 v[50:53], v[212:215], v[180:183], v[50:53] cbsz:4 blgp:4
	v_mfma_f32_16x16x128_f8f6f4 v[50:53], v[220:223], v[188:191], v[50:53] cbsz:4 blgp:4
	v_mfma_f32_16x16x128_f8f6f4 v[54:57], v[216:219], v[180:183], v[54:57] cbsz:4 blgp:4
	v_mfma_f32_16x16x128_f8f6f4 v[54:57], v[224:227], v[188:191], v[54:57] cbsz:4 blgp:4
	v_mfma_f32_16x16x128_f8f6f4 v[58:61], v[212:215], v[184:187], v[58:61] cbsz:4 blgp:4
	v_mfma_f32_16x16x128_f8f6f4 v[58:61], v[220:223], v[192:195], v[58:61] cbsz:4 blgp:4
	v_mfma_f32_16x16x128_f8f6f4 v[62:65], v[216:219], v[184:187], v[62:65] cbsz:4 blgp:4
	v_mfma_f32_16x16x128_f8f6f4 v[62:65], v[224:227], v[192:195], v[62:65] cbsz:4 blgp:4
	v_mfma_f32_16x16x128_f8f6f4 v[66:69], v[212:215], v[196:199], v[66:69] cbsz:4 blgp:4
	v_mfma_f32_16x16x128_f8f6f4 v[66:69], v[220:223], v[204:207], v[66:69] cbsz:4 blgp:4
	v_mfma_f32_16x16x128_f8f6f4 v[70:73], v[216:219], v[196:199], v[70:73] cbsz:4 blgp:4
	v_mfma_f32_16x16x128_f8f6f4 v[70:73], v[224:227], v[204:207], v[70:73] cbsz:4 blgp:4
	v_mfma_f32_16x16x128_f8f6f4 v[74:77], v[212:215], v[200:203], v[74:77] cbsz:4 blgp:4
	v_mfma_f32_16x16x128_f8f6f4 v[74:77], v[220:223], v[208:211], v[74:77] cbsz:4 blgp:4
	v_mfma_f32_16x16x128_f8f6f4 v[78:81], v[216:219], v[200:203], v[78:81] cbsz:4 blgp:4
	v_mfma_f32_16x16x128_f8f6f4 v[78:81], v[224:227], v[208:211], v[78:81] cbsz:4 blgp:4
	s_setprio 0
	s_barrier
	s_mov_b32 m0, s65
	s_nop 0
	global_load_lds_dwordx4 v148, s[42:43]
	s_mov_b32 m0, s66
	s_nop 0
	global_load_lds_dwordx4 v152, s[42:43]
	ds_read_b128 v[180:183], v165 offset:49152
	ds_read_b128 v[184:187], v165 offset:51200
	ds_read_b128 v[188:191], v166 offset:49152
	ds_read_b128 v[192:195], v166 offset:51200
	ds_read_b128 v[196:199], v165 offset:53248
	ds_read_b128 v[200:203], v165 offset:55296
	ds_read_b128 v[204:207], v166 offset:53248
	ds_read_b128 v[208:211], v166 offset:55296
	s_mov_b32 m0, s67
	s_nop 0
	global_load_lds_dwordx4 v146, s[46:47]
	s_mov_b32 m0, s68
	s_nop 0
	global_load_lds_dwordx4 v150, s[46:47]
	s_add_u32 s42, s42, s24
	s_addc_u32 s43, s43, s25
	s_mov_b32 m0, s69
	s_nop 0
	global_load_lds_dwordx4 v148, s[42:43]
	s_mov_b32 m0, s70
	s_nop 0
	global_load_lds_dwordx4 v152, s[42:43]
	s_waitcnt vmcnt(8)
	s_waitcnt lgkmcnt(0)
	s_barrier
	s_setprio 1
	v_mfma_f32_16x16x128_f8f6f4 v[86:89], v[156:159], v[180:183], v[86:89] cbsz:4 blgp:4
	v_mfma_f32_16x16x128_f8f6f4 v[86:89], v[172:175], v[188:191], v[86:89] cbsz:4 blgp:4
	v_mfma_f32_16x16x128_f8f6f4 v[90:93], v[168:171], v[180:183], v[90:93] cbsz:4 blgp:4
	v_mfma_f32_16x16x128_f8f6f4 v[90:93], v[176:179], v[188:191], v[90:93] cbsz:4 blgp:4
	v_mfma_f32_16x16x128_f8f6f4 v[98:101], v[156:159], v[184:187], v[98:101] cbsz:4 blgp:4
	v_mfma_f32_16x16x128_f8f6f4 v[98:101], v[172:175], v[192:195], v[98:101] cbsz:4 blgp:4
	v_mfma_f32_16x16x128_f8f6f4 v[106:109], v[168:171], v[184:187], v[106:109] cbsz:4 blgp:4
	v_mfma_f32_16x16x128_f8f6f4 v[106:109], v[176:179], v[192:195], v[106:109] cbsz:4 blgp:4
	v_mfma_f32_16x16x128_f8f6f4 v[118:121], v[156:159], v[196:199], v[118:121] cbsz:4 blgp:4
	v_mfma_f32_16x16x128_f8f6f4 v[118:121], v[172:175], v[204:207], v[118:121] cbsz:4 blgp:4
	v_mfma_f32_16x16x128_f8f6f4 v[126:129], v[168:171], v[196:199], v[126:129] cbsz:4 blgp:4
	v_mfma_f32_16x16x128_f8f6f4 v[126:129], v[176:179], v[204:207], v[126:129] cbsz:4 blgp:4
	v_mfma_f32_16x16x128_f8f6f4 v[138:141], v[156:159], v[200:203], v[138:141] cbsz:4 blgp:4
	v_mfma_f32_16x16x128_f8f6f4 v[138:141], v[172:175], v[208:211], v[138:141] cbsz:4 blgp:4
	v_mfma_f32_16x16x128_f8f6f4 v[82:85], v[168:171], v[200:203], v[82:85] cbsz:4 blgp:4
	v_mfma_f32_16x16x128_f8f6f4 v[82:85], v[176:179], v[208:211], v[82:85] cbsz:4 blgp:4
	v_mfma_f32_16x16x128_f8f6f4 v[94:97], v[212:215], v[180:183], v[94:97] cbsz:4 blgp:4
	v_mfma_f32_16x16x128_f8f6f4 v[94:97], v[220:223], v[188:191], v[94:97] cbsz:4 blgp:4
	v_mfma_f32_16x16x128_f8f6f4 v[102:105], v[216:219], v[180:183], v[102:105] cbsz:4 blgp:4
	v_mfma_f32_16x16x128_f8f6f4 v[102:105], v[224:227], v[188:191], v[102:105] cbsz:4 blgp:4
	v_mfma_f32_16x16x128_f8f6f4 v[110:113], v[212:215], v[184:187], v[110:113] cbsz:4 blgp:4
	v_mfma_f32_16x16x128_f8f6f4 v[110:113], v[220:223], v[192:195], v[110:113] cbsz:4 blgp:4
	v_mfma_f32_16x16x128_f8f6f4 v[114:117], v[216:219], v[184:187], v[114:117] cbsz:4 blgp:4
	v_mfma_f32_16x16x128_f8f6f4 v[114:117], v[224:227], v[192:195], v[114:117] cbsz:4 blgp:4
	v_mfma_f32_16x16x128_f8f6f4 v[122:125], v[212:215], v[196:199], v[122:125] cbsz:4 blgp:4
	v_mfma_f32_16x16x128_f8f6f4 v[122:125], v[220:223], v[204:207], v[122:125] cbsz:4 blgp:4
	v_mfma_f32_16x16x128_f8f6f4 v[130:133], v[216:219], v[196:199], v[130:133] cbsz:4 blgp:4
	v_mfma_f32_16x16x128_f8f6f4 v[130:133], v[224:227], v[204:207], v[130:133] cbsz:4 blgp:4
	v_mfma_f32_16x16x128_f8f6f4 v[134:137], v[212:215], v[200:203], v[134:137] cbsz:4 blgp:4
	v_mfma_f32_16x16x128_f8f6f4 v[134:137], v[220:223], v[208:211], v[134:137] cbsz:4 blgp:4
	v_mfma_f32_16x16x128_f8f6f4 v[142:145], v[216:219], v[200:203], v[142:145] cbsz:4 blgp:4
	v_mfma_f32_16x16x128_f8f6f4 v[142:145], v[224:227], v[208:211], v[142:145] cbsz:4 blgp:4
	s_setprio 0
	s_add_i32 s42, s82, 2
	s_add_u32 s29, s29, 0x100
	s_addc_u32 s79, s79, 0
	s_add_u32 s80, s80, 0x100
	s_addc_u32 s81, s81, 0
	s_add_u32 s40, s40, 0x100
	s_addc_u32 s41, s41, 0
	s_cmp_ge_i32 s82, s64
	s_barrier
	s_cbranch_scc1 .LBB5_4
	s_mov_b32 s82, s42
	s_cmp_eq_u32 s64, s82
	s_cselect_b64 s[42:43], -1, 0
	s_cmp_lg_u32 s64, s82
	s_cbranch_scc0 .LBB5_14
	s_branch .LBB5_15

.LBB6_15:
	s_add_u32 s82, s36, s20
	s_addc_u32 s83, s37, s21
	s_add_u32 s31, s36, 0x100
	s_addc_u32 s39, s37, 0
	s_and_b64 s[40:41], s[12:13], exec
	ds_read_b128 v[82:85], v169
	ds_read_b128 v[94:97], v169 offset:2048
	ds_read_b128 v[102:105], v178
	ds_read_b128 v[110:113], v178 offset:2048
	s_cselect_b32 s45, s5, s39
	s_cselect_b32 s44, s4, s31
	s_add_u32 s31, s34, 0x100
	s_addc_u32 s39, s35, 0
	s_and_b64 s[40:41], s[12:13], exec
	s_cselect_b32 s47, s7, s39
	s_cselect_b32 s46, s6, s31
	s_add_u32 s42, s44, 0x80
	s_addc_u32 s43, s45, 0
	s_add_u32 s40, s46, 0x80
	s_addc_u32 s41, s47, 0
	ds_read_b128 v[58:61], v179
	ds_read_b128 v[66:69], v179 offset:2048
	ds_read_b128 v[62:65], v180
	ds_read_b128 v[70:73], v180 offset:2048
	ds_read_b128 v[74:77], v179 offset:4096
	ds_read_b128 v[86:89], v179 offset:6144
	ds_read_b128 v[78:81], v180 offset:4096
	ds_read_b128 v[90:93], v180 offset:6144
	s_add_u32 s84, s82, 0x80
	s_addc_u32 s85, s83, 0
	s_mov_b32 m0, s68
	s_nop 0
	global_load_lds_dwordx4 v162, s[84:85]
	s_mov_b32 m0, s69
	s_nop 0
	global_load_lds_dwordx4 v166, s[84:85]
	s_waitcnt lgkmcnt(8)
	ds_read_b128 v[142:145], v169 offset:16384
	ds_read_b128 v[146:149], v169 offset:18432
	ds_read_b128 v[150:153], v178 offset:16384
	ds_read_b128 v[154:157], v178 offset:18432
	s_waitcnt vmcnt(8)
	s_waitcnt lgkmcnt(0)
	s_barrier
	s_waitcnt lgkmcnt(0)
	s_waitcnt vmcnt(16)
	v_mov_b32_e32 v171, v170
	v_pk_mul_f32 v[16:17], v[170:171], v[16:17]
	v_pk_mul_f32 v[14:15], v[172:173], v[14:15]
	v_pk_mul_f32 v[12:13], v[170:171], v[12:13]
	v_pk_mul_f32 v[10:11], v[172:173], v[10:11]
	v_pk_mul_f32 v[8:9], v[170:171], v[8:9]
	v_pk_mul_f32 v[6:7], v[172:173], v[6:7]
	v_pk_mul_f32 v[4:5], v[170:171], v[4:5]
	v_pk_mul_f32 v[2:3], v[172:173], v[2:3]
	s_setprio 1
	v_mfma_f32_16x16x128_f8f6f4 v[18:21], v[82:85], v[58:61], v[14:17] cbsz:4 blgp:4
	v_mfma_f32_16x16x128_f8f6f4 v[18:21], v[102:105], v[62:65], v[18:21] cbsz:4 blgp:4
	v_mfma_f32_16x16x128_f8f6f4 v[22:25], v[94:97], v[58:61], v[10:13] cbsz:4 blgp:4
	v_mfma_f32_16x16x128_f8f6f4 v[22:25], v[110:113], v[62:65], v[22:25] cbsz:4 blgp:4
	v_mfma_f32_16x16x128_f8f6f4 v[26:29], v[82:85], v[66:69], v[14:17] cbsz:4 blgp:4
	v_mfma_f32_16x16x128_f8f6f4 v[26:29], v[102:105], v[70:73], v[26:29] cbsz:4 blgp:4
	v_mfma_f32_16x16x128_f8f6f4 v[30:33], v[94:97], v[66:69], v[10:13] cbsz:4 blgp:4
	v_mfma_f32_16x16x128_f8f6f4 v[30:33], v[110:113], v[70:73], v[30:33] cbsz:4 blgp:4
	v_mfma_f32_16x16x128_f8f6f4 v[34:37], v[82:85], v[74:77], v[14:17] cbsz:4 blgp:4
	v_mfma_f32_16x16x128_f8f6f4 v[34:37], v[102:105], v[78:81], v[34:37] cbsz:4 blgp:4
	v_mfma_f32_16x16x128_f8f6f4 v[38:41], v[94:97], v[74:77], v[10:13] cbsz:4 blgp:4
	v_mfma_f32_16x16x128_f8f6f4 v[38:41], v[110:113], v[78:81], v[38:41] cbsz:4 blgp:4
	v_mfma_f32_16x16x128_f8f6f4 v[42:45], v[82:85], v[86:89], v[14:17] cbsz:4 blgp:4
	v_mfma_f32_16x16x128_f8f6f4 v[42:45], v[102:105], v[90:93], v[42:45] cbsz:4 blgp:4
	v_mfma_f32_16x16x128_f8f6f4 v[46:49], v[94:97], v[86:89], v[10:13] cbsz:4 blgp:4
	v_mfma_f32_16x16x128_f8f6f4 v[46:49], v[110:113], v[90:93], v[46:49] cbsz:4 blgp:4
	v_mfma_f32_16x16x128_f8f6f4 v[50:53], v[142:145], v[58:61], v[6:9] cbsz:4 blgp:4
	v_mfma_f32_16x16x128_f8f6f4 v[50:53], v[150:153], v[62:65], v[50:53] cbsz:4 blgp:4
	v_mfma_f32_16x16x128_f8f6f4 v[54:57], v[146:149], v[58:61], v[2:5] cbsz:4 blgp:4
	v_mfma_f32_16x16x128_f8f6f4 v[54:57], v[154:157], v[62:65], v[54:57] cbsz:4 blgp:4
	v_mfma_f32_16x16x128_f8f6f4 v[58:61], v[142:145], v[66:69], v[6:9] cbsz:4 blgp:4
	v_mfma_f32_16x16x128_f8f6f4 v[58:61], v[150:153], v[70:73], v[58:61] cbsz:4 blgp:4
	v_mfma_f32_16x16x128_f8f6f4 v[62:65], v[146:149], v[66:69], v[2:5] cbsz:4 blgp:4
	v_mfma_f32_16x16x128_f8f6f4 v[62:65], v[154:157], v[70:73], v[62:65] cbsz:4 blgp:4
	v_mfma_f32_16x16x128_f8f6f4 v[66:69], v[142:145], v[74:77], v[6:9] cbsz:4 blgp:4
	v_mfma_f32_16x16x128_f8f6f4 v[66:69], v[150:153], v[78:81], v[66:69] cbsz:4 blgp:4
	v_mfma_f32_16x16x128_f8f6f4 v[70:73], v[146:149], v[74:77], v[2:5] cbsz:4 blgp:4
	v_mfma_f32_16x16x128_f8f6f4 v[70:73], v[154:157], v[78:81], v[70:73] cbsz:4 blgp:4
	v_mfma_f32_16x16x128_f8f6f4 v[74:77], v[142:145], v[86:89], v[6:9] cbsz:4 blgp:4
	v_mfma_f32_16x16x128_f8f6f4 v[74:77], v[150:153], v[90:93], v[74:77] cbsz:4 blgp:4
	v_mfma_f32_16x16x128_f8f6f4 v[78:81], v[146:149], v[86:89], v[2:5] cbsz:4 blgp:4
	v_mfma_f32_16x16x128_f8f6f4 v[78:81], v[154:157], v[90:93], v[78:81] cbsz:4 blgp:4
	s_setprio 0
	s_barrier
	s_mov_b32 m0, s54
	s_nop 0
	global_load_lds_dwordx4 v164, s[46:47]
	s_mov_b32 m0, s55
	s_nop 0
	global_load_lds_dwordx4 v168, s[46:47]
	ds_read_b128 v[114:117], v179 offset:16384
	ds_read_b128 v[122:125], v179 offset:18432
	ds_read_b128 v[130:133], v180 offset:16384
	ds_read_b128 v[134:137], v180 offset:18432
	ds_read_b128 v[158:161], v179 offset:20480
	ds_read_b128 v[182:185], v179 offset:22528
	ds_read_b128 v[186:189], v180 offset:20480
	ds_read_b128 v[190:193], v180 offset:22528
	s_mov_b32 m0, s53
	s_nop 0
	global_load_lds_dwordx4 v162, s[44:45]
	s_mov_b32 m0, s56
	s_nop 0
	global_load_lds_dwordx4 v166, s[44:45]
	s_add_u32 s46, s46, s22
	s_addc_u32 s47, s47, s23
	s_mov_b32 m0, s57
	s_nop 0
	global_load_lds_dwordx4 v164, s[46:47]
	s_mov_b32 m0, s58
	s_nop 0
	global_load_lds_dwordx4 v168, s[46:47]
	s_waitcnt vmcnt(8)
	s_waitcnt lgkmcnt(0)
	s_barrier
	s_setprio 1
	v_mfma_f32_16x16x128_f8f6f4 v[86:89], v[82:85], v[114:117], v[14:17] cbsz:4 blgp:4
	v_mfma_f32_16x16x128_f8f6f4 v[86:89], v[102:105], v[130:133], v[86:89] cbsz:4 blgp:4
	v_mfma_f32_16x16x128_f8f6f4 v[90:93], v[94:97], v[114:117], v[10:13] cbsz:4 blgp:4
	v_mfma_f32_16x16x128_f8f6f4 v[90:93], v[110:113], v[130:133], v[90:93] cbsz:4 blgp:4
	v_mfma_f32_16x16x128_f8f6f4 v[98:101], v[82:85], v[122:125], v[14:17] cbsz:4 blgp:4
	v_mfma_f32_16x16x128_f8f6f4 v[98:101], v[102:105], v[134:137], v[98:101] cbsz:4 blgp:4
	v_mfma_f32_16x16x128_f8f6f4 v[106:109], v[94:97], v[122:125], v[10:13] cbsz:4 blgp:4
	v_mfma_f32_16x16x128_f8f6f4 v[106:109], v[110:113], v[134:137], v[106:109] cbsz:4 blgp:4
	v_mfma_f32_16x16x128_f8f6f4 v[118:121], v[82:85], v[158:161], v[14:17] cbsz:4 blgp:4
	v_mfma_f32_16x16x128_f8f6f4 v[118:121], v[102:105], v[186:189], v[118:121] cbsz:4 blgp:4
	v_mfma_f32_16x16x128_f8f6f4 v[126:129], v[94:97], v[158:161], v[10:13] cbsz:4 blgp:4
	v_mfma_f32_16x16x128_f8f6f4 v[126:129], v[110:113], v[186:189], v[126:129] cbsz:4 blgp:4
	v_mfma_f32_16x16x128_f8f6f4 v[138:141], v[82:85], v[182:185], v[14:17] cbsz:4 blgp:4
	v_mfma_f32_16x16x128_f8f6f4 v[138:141], v[102:105], v[190:193], v[138:141] cbsz:4 blgp:4
	v_mfma_f32_16x16x128_f8f6f4 v[82:85], v[94:97], v[182:185], v[10:13] cbsz:4 blgp:4
	v_mfma_f32_16x16x128_f8f6f4 v[82:85], v[110:113], v[190:193], v[82:85] cbsz:4 blgp:4
	v_mfma_f32_16x16x128_f8f6f4 v[94:97], v[142:145], v[114:117], v[6:9] cbsz:4 blgp:4
	v_mfma_f32_16x16x128_f8f6f4 v[94:97], v[150:153], v[130:133], v[94:97] cbsz:4 blgp:4
	v_mfma_f32_16x16x128_f8f6f4 v[102:105], v[146:149], v[114:117], v[2:5] cbsz:4 blgp:4
	v_mfma_f32_16x16x128_f8f6f4 v[102:105], v[154:157], v[130:133], v[102:105] cbsz:4 blgp:4
	v_mfma_f32_16x16x128_f8f6f4 v[110:113], v[142:145], v[122:125], v[6:9] cbsz:4 blgp:4
	v_mfma_f32_16x16x128_f8f6f4 v[110:113], v[150:153], v[134:137], v[110:113] cbsz:4 blgp:4
	v_mfma_f32_16x16x128_f8f6f4 v[114:117], v[146:149], v[122:125], v[2:5] cbsz:4 blgp:4
	v_mfma_f32_16x16x128_f8f6f4 v[114:117], v[154:157], v[134:137], v[114:117] cbsz:4 blgp:4
	v_mfma_f32_16x16x128_f8f6f4 v[122:125], v[142:145], v[158:161], v[6:9] cbsz:4 blgp:4
	v_mfma_f32_16x16x128_f8f6f4 v[122:125], v[150:153], v[186:189], v[122:125] cbsz:4 blgp:4
	v_mfma_f32_16x16x128_f8f6f4 v[130:133], v[146:149], v[158:161], v[2:5] cbsz:4 blgp:4
	v_mfma_f32_16x16x128_f8f6f4 v[130:133], v[154:157], v[186:189], v[130:133] cbsz:4 blgp:4
	v_mfma_f32_16x16x128_f8f6f4 v[134:137], v[142:145], v[182:185], v[6:9] cbsz:4 blgp:4
	v_mfma_f32_16x16x128_f8f6f4 v[134:137], v[150:153], v[190:193], v[134:137] cbsz:4 blgp:4
	v_mfma_f32_16x16x128_f8f6f4 v[142:145], v[146:149], v[182:185], v[2:5] cbsz:4 blgp:4
	v_mfma_f32_16x16x128_f8f6f4 v[142:145], v[154:157], v[190:193], v[142:145] cbsz:4 blgp:4
	s_setprio 0
	s_barrier
	ds_read_b128 v[146:149], v169 offset:32768
	ds_read_b128 v[150:153], v169 offset:34816
	ds_read_b128 v[154:157], v178 offset:32768
	ds_read_b128 v[158:161], v178 offset:34816
	ds_read_b128 v[182:185], v179 offset:32768
	ds_read_b128 v[186:189], v179 offset:34816
	ds_read_b128 v[190:193], v180 offset:32768
	ds_read_b128 v[194:197], v180 offset:34816
	ds_read_b128 v[198:201], v179 offset:36864
	ds_read_b128 v[202:205], v179 offset:38912
	ds_read_b128 v[206:209], v180 offset:36864
	ds_read_b128 v[210:213], v180 offset:38912
	s_add_u32 s44, s44, s20
	s_addc_u32 s45, s45, s21
	s_mov_b32 m0, s59
	s_nop 0
	global_load_lds_dwordx4 v162, s[44:45]
	s_mov_b32 m0, s60
	s_nop 0
	global_load_lds_dwordx4 v166, s[44:45]
	s_waitcnt lgkmcnt(8)
	ds_read_b128 v[214:217], v169 offset:49152
	ds_read_b128 v[218:221], v169 offset:51200
	ds_read_b128 v[222:225], v178 offset:49152
	ds_read_b128 v[226:229], v178 offset:51200
	s_waitcnt vmcnt(8)
	s_waitcnt lgkmcnt(0)
	s_barrier
	s_waitcnt lgkmcnt(0)
	s_setprio 1
	v_mfma_f32_16x16x128_f8f6f4 v[18:21], v[146:149], v[182:185], v[18:21] cbsz:4 blgp:4
	v_mfma_f32_16x16x128_f8f6f4 v[18:21], v[154:157], v[190:193], v[18:21] cbsz:4 blgp:4
	v_mfma_f32_16x16x128_f8f6f4 v[22:25], v[150:153], v[182:185], v[22:25] cbsz:4 blgp:4
	v_mfma_f32_16x16x128_f8f6f4 v[22:25], v[158:161], v[190:193], v[22:25] cbsz:4 blgp:4
	v_mfma_f32_16x16x128_f8f6f4 v[26:29], v[146:149], v[186:189], v[26:29] cbsz:4 blgp:4
	v_mfma_f32_16x16x128_f8f6f4 v[26:29], v[154:157], v[194:197], v[26:29] cbsz:4 blgp:4
	v_mfma_f32_16x16x128_f8f6f4 v[30:33], v[150:153], v[186:189], v[30:33] cbsz:4 blgp:4
	v_mfma_f32_16x16x128_f8f6f4 v[30:33], v[158:161], v[194:197], v[30:33] cbsz:4 blgp:4
	v_mfma_f32_16x16x128_f8f6f4 v[34:37], v[146:149], v[198:201], v[34:37] cbsz:4 blgp:4
	v_mfma_f32_16x16x128_f8f6f4 v[34:37], v[154:157], v[206:209], v[34:37] cbsz:4 blgp:4
	v_mfma_f32_16x16x128_f8f6f4 v[38:41], v[150:153], v[198:201], v[38:41] cbsz:4 blgp:4
	v_mfma_f32_16x16x128_f8f6f4 v[38:41], v[158:161], v[206:209], v[38:41] cbsz:4 blgp:4
	v_mfma_f32_16x16x128_f8f6f4 v[42:45], v[146:149], v[202:205], v[42:45] cbsz:4 blgp:4
	v_mfma_f32_16x16x128_f8f6f4 v[42:45], v[154:157], v[210:213], v[42:45] cbsz:4 blgp:4
	v_mfma_f32_16x16x128_f8f6f4 v[46:49], v[150:153], v[202:205], v[46:49] cbsz:4 blgp:4
	v_mfma_f32_16x16x128_f8f6f4 v[46:49], v[158:161], v[210:213], v[46:49] cbsz:4 blgp:4
	v_mfma_f32_16x16x128_f8f6f4 v[50:53], v[214:217], v[182:185], v[50:53] cbsz:4 blgp:4
	v_mfma_f32_16x16x128_f8f6f4 v[50:53], v[222:225], v[190:193], v[50:53] cbsz:4 blgp:4
	v_mfma_f32_16x16x128_f8f6f4 v[54:57], v[218:221], v[182:185], v[54:57] cbsz:4 blgp:4
	v_mfma_f32_16x16x128_f8f6f4 v[54:57], v[226:229], v[190:193], v[54:57] cbsz:4 blgp:4
	v_mfma_f32_16x16x128_f8f6f4 v[58:61], v[214:217], v[186:189], v[58:61] cbsz:4 blgp:4
	v_mfma_f32_16x16x128_f8f6f4 v[58:61], v[222:225], v[194:197], v[58:61] cbsz:4 blgp:4
	v_mfma_f32_16x16x128_f8f6f4 v[62:65], v[218:221], v[186:189], v[62:65] cbsz:4 blgp:4
	v_mfma_f32_16x16x128_f8f6f4 v[62:65], v[226:229], v[194:197], v[62:65] cbsz:4 blgp:4
	v_mfma_f32_16x16x128_f8f6f4 v[66:69], v[214:217], v[198:201], v[66:69] cbsz:4 blgp:4
	v_mfma_f32_16x16x128_f8f6f4 v[66:69], v[222:225], v[206:209], v[66:69] cbsz:4 blgp:4
	v_mfma_f32_16x16x128_f8f6f4 v[70:73], v[218:221], v[198:201], v[70:73] cbsz:4 blgp:4
	v_mfma_f32_16x16x128_f8f6f4 v[70:73], v[226:229], v[206:209], v[70:73] cbsz:4 blgp:4
	v_mfma_f32_16x16x128_f8f6f4 v[74:77], v[214:217], v[202:205], v[74:77] cbsz:4 blgp:4
	v_mfma_f32_16x16x128_f8f6f4 v[74:77], v[222:225], v[210:213], v[74:77] cbsz:4 blgp:4
	v_mfma_f32_16x16x128_f8f6f4 v[78:81], v[218:221], v[202:205], v[78:81] cbsz:4 blgp:4
	v_mfma_f32_16x16x128_f8f6f4 v[78:81], v[226:229], v[210:213], v[78:81] cbsz:4 blgp:4
	s_setprio 0
	s_barrier
	s_mov_b32 m0, s62
	s_nop 0
	global_load_lds_dwordx4 v164, s[40:41]
	s_mov_b32 m0, s63
	s_nop 0
	global_load_lds_dwordx4 v168, s[40:41]
	ds_read_b128 v[182:185], v179 offset:49152
	ds_read_b128 v[186:189], v179 offset:51200
	ds_read_b128 v[190:193], v180 offset:49152
	ds_read_b128 v[194:197], v180 offset:51200
	ds_read_b128 v[198:201], v179 offset:53248
	ds_read_b128 v[202:205], v179 offset:55296
	ds_read_b128 v[206:209], v180 offset:53248
	ds_read_b128 v[210:213], v180 offset:55296
	s_mov_b32 m0, s64
	s_nop 0
	global_load_lds_dwordx4 v162, s[42:43]
	s_mov_b32 m0, s65
	s_nop 0
	global_load_lds_dwordx4 v166, s[42:43]
	s_add_u32 s40, s40, s22
	s_addc_u32 s41, s41, s23
	s_mov_b32 m0, s66
	s_nop 0
	global_load_lds_dwordx4 v164, s[40:41]
	s_mov_b32 m0, s67
	s_nop 0
	global_load_lds_dwordx4 v168, s[40:41]
	s_waitcnt vmcnt(8)
	s_waitcnt lgkmcnt(0)
	s_barrier
	s_setprio 1
	v_mfma_f32_16x16x128_f8f6f4 v[86:89], v[146:149], v[182:185], v[86:89] cbsz:4 blgp:4
	v_mfma_f32_16x16x128_f8f6f4 v[86:89], v[154:157], v[190:193], v[86:89] cbsz:4 blgp:4
	v_mfma_f32_16x16x128_f8f6f4 v[90:93], v[150:153], v[182:185], v[90:93] cbsz:4 blgp:4
	v_mfma_f32_16x16x128_f8f6f4 v[90:93], v[158:161], v[190:193], v[90:93] cbsz:4 blgp:4
	v_mfma_f32_16x16x128_f8f6f4 v[98:101], v[146:149], v[186:189], v[98:101] cbsz:4 blgp:4
	v_mfma_f32_16x16x128_f8f6f4 v[98:101], v[154:157], v[194:197], v[98:101] cbsz:4 blgp:4
	v_mfma_f32_16x16x128_f8f6f4 v[106:109], v[150:153], v[186:189], v[106:109] cbsz:4 blgp:4
	v_mfma_f32_16x16x128_f8f6f4 v[106:109], v[158:161], v[194:197], v[106:109] cbsz:4 blgp:4
	v_mfma_f32_16x16x128_f8f6f4 v[118:121], v[146:149], v[198:201], v[118:121] cbsz:4 blgp:4
	v_mfma_f32_16x16x128_f8f6f4 v[118:121], v[154:157], v[206:209], v[118:121] cbsz:4 blgp:4
	v_mfma_f32_16x16x128_f8f6f4 v[126:129], v[150:153], v[198:201], v[126:129] cbsz:4 blgp:4
	v_mfma_f32_16x16x128_f8f6f4 v[126:129], v[158:161], v[206:209], v[126:129] cbsz:4 blgp:4
	v_mfma_f32_16x16x128_f8f6f4 v[138:141], v[146:149], v[202:205], v[138:141] cbsz:4 blgp:4
	v_mfma_f32_16x16x128_f8f6f4 v[138:141], v[154:157], v[210:213], v[138:141] cbsz:4 blgp:4
	v_mfma_f32_16x16x128_f8f6f4 v[82:85], v[150:153], v[202:205], v[82:85] cbsz:4 blgp:4
	v_mfma_f32_16x16x128_f8f6f4 v[82:85], v[158:161], v[210:213], v[82:85] cbsz:4 blgp:4
	v_mfma_f32_16x16x128_f8f6f4 v[94:97], v[214:217], v[182:185], v[94:97] cbsz:4 blgp:4
	v_mfma_f32_16x16x128_f8f6f4 v[94:97], v[222:225], v[190:193], v[94:97] cbsz:4 blgp:4
	v_mfma_f32_16x16x128_f8f6f4 v[102:105], v[218:221], v[182:185], v[102:105] cbsz:4 blgp:4
	v_mfma_f32_16x16x128_f8f6f4 v[102:105], v[226:229], v[190:193], v[102:105] cbsz:4 blgp:4
	v_mfma_f32_16x16x128_f8f6f4 v[110:113], v[214:217], v[186:189], v[110:113] cbsz:4 blgp:4
	v_mfma_f32_16x16x128_f8f6f4 v[110:113], v[222:225], v[194:197], v[110:113] cbsz:4 blgp:4
	v_mfma_f32_16x16x128_f8f6f4 v[114:117], v[218:221], v[186:189], v[114:117] cbsz:4 blgp:4
	v_mfma_f32_16x16x128_f8f6f4 v[114:117], v[226:229], v[194:197], v[114:117] cbsz:4 blgp:4
	v_mfma_f32_16x16x128_f8f6f4 v[122:125], v[214:217], v[198:201], v[122:125] cbsz:4 blgp:4
	v_mfma_f32_16x16x128_f8f6f4 v[122:125], v[222:225], v[206:209], v[122:125] cbsz:4 blgp:4
	v_mfma_f32_16x16x128_f8f6f4 v[130:133], v[218:221], v[198:201], v[130:133] cbsz:4 blgp:4
	v_mfma_f32_16x16x128_f8f6f4 v[130:133], v[226:229], v[206:209], v[130:133] cbsz:4 blgp:4
	v_mfma_f32_16x16x128_f8f6f4 v[134:137], v[214:217], v[202:205], v[134:137] cbsz:4 blgp:4
	v_mfma_f32_16x16x128_f8f6f4 v[134:137], v[222:225], v[210:213], v[134:137] cbsz:4 blgp:4
	v_mfma_f32_16x16x128_f8f6f4 v[142:145], v[218:221], v[202:205], v[142:145] cbsz:4 blgp:4
	v_mfma_f32_16x16x128_f8f6f4 v[142:145], v[226:229], v[210:213], v[142:145] cbsz:4 blgp:4
	s_setprio 0
	s_andn2_b64 vcc, exec, s[28:29]
	s_barrier
	s_cbranch_vccnz .LBB6_20
	s_ashr_i32 s39, s38, 31
	s_lshl_b64 s[38:39], s[38:39], 10
	s_add_u32 s38, s14, s38
	s_addc_u32 s39, s15, s39
	s_add_u32 s31, s36, 0x200
	s_addc_u32 s46, s37, 0
	s_add_u32 s47, s34, 0x200
	s_addc_u32 s81, s35, 0
	s_add_u32 s34, s82, 0x180
	s_addc_u32 s35, s83, 0
	s_mov_b32 s82, 4
	s_cmp_eq_u32 s61, s82
	s_cselect_b64 s[36:37], -1, 0
	s_cmp_lg_u32 s61, s82
	s_cbranch_scc1 .LBB6_18

.LBB6_18:
	ds_read_b128 v[146:149], v169
	ds_read_b128 v[150:153], v169 offset:2048
	ds_read_b128 v[154:157], v178
	ds_read_b128 v[158:161], v178 offset:2048
	s_and_b64 s[36:37], s[36:37], exec
	s_cselect_b32 s42, s4, s31
	s_cselect_b32 s43, s5, s46
	s_cselect_b32 s45, s7, s81
	s_cselect_b32 s44, s6, s47
	s_add_u32 s40, s42, 0x80
	s_addc_u32 s41, s43, 0
	s_add_u32 s36, s44, 0x80
	s_addc_u32 s37, s45, 0
	ds_read_b128 v[182:185], v179
	ds_read_b128 v[186:189], v179 offset:2048
	ds_read_b128 v[190:193], v180
	ds_read_b128 v[194:197], v180 offset:2048
	ds_read_b128 v[198:201], v179 offset:4096
	ds_read_b128 v[202:205], v179 offset:6144
	ds_read_b128 v[206:209], v180 offset:4096
	ds_read_b128 v[210:213], v180 offset:6144
	s_mov_b32 m0, s68
	s_nop 0
	global_load_lds_dwordx4 v162, s[34:35]
	s_mov_b32 m0, s69
	s_nop 0
	global_load_lds_dwordx4 v166, s[34:35]
	s_waitcnt lgkmcnt(8)
	ds_read_b128 v[214:217], v169 offset:16384
	ds_read_b128 v[218:221], v169 offset:18432
	ds_read_b128 v[222:225], v178 offset:16384
	ds_read_b128 v[226:229], v178 offset:18432
	s_waitcnt vmcnt(8)
	s_waitcnt lgkmcnt(0)
	s_barrier
	s_waitcnt lgkmcnt(0)
	s_setprio 1
	v_mfma_f32_16x16x128_f8f6f4 v[18:21], v[146:149], v[182:185], v[18:21] cbsz:4 blgp:4
	v_mfma_f32_16x16x128_f8f6f4 v[18:21], v[154:157], v[190:193], v[18:21] cbsz:4 blgp:4
	v_mfma_f32_16x16x128_f8f6f4 v[22:25], v[150:153], v[182:185], v[22:25] cbsz:4 blgp:4
	v_mfma_f32_16x16x128_f8f6f4 v[22:25], v[158:161], v[190:193], v[22:25] cbsz:4 blgp:4
	v_mfma_f32_16x16x128_f8f6f4 v[26:29], v[146:149], v[186:189], v[26:29] cbsz:4 blgp:4
	v_mfma_f32_16x16x128_f8f6f4 v[26:29], v[154:157], v[194:197], v[26:29] cbsz:4 blgp:4
	v_mfma_f32_16x16x128_f8f6f4 v[30:33], v[150:153], v[186:189], v[30:33] cbsz:4 blgp:4
	v_mfma_f32_16x16x128_f8f6f4 v[30:33], v[158:161], v[194:197], v[30:33] cbsz:4 blgp:4
	v_mfma_f32_16x16x128_f8f6f4 v[34:37], v[146:149], v[198:201], v[34:37] cbsz:4 blgp:4
	v_mfma_f32_16x16x128_f8f6f4 v[34:37], v[154:157], v[206:209], v[34:37] cbsz:4 blgp:4
	v_mfma_f32_16x16x128_f8f6f4 v[38:41], v[150:153], v[198:201], v[38:41] cbsz:4 blgp:4
	v_mfma_f32_16x16x128_f8f6f4 v[38:41], v[158:161], v[206:209], v[38:41] cbsz:4 blgp:4
	v_mfma_f32_16x16x128_f8f6f4 v[42:45], v[146:149], v[202:205], v[42:45] cbsz:4 blgp:4
	v_mfma_f32_16x16x128_f8f6f4 v[42:45], v[154:157], v[210:213], v[42:45] cbsz:4 blgp:4
	v_mfma_f32_16x16x128_f8f6f4 v[46:49], v[150:153], v[202:205], v[46:49] cbsz:4 blgp:4
	v_mfma_f32_16x16x128_f8f6f4 v[46:49], v[158:161], v[210:213], v[46:49] cbsz:4 blgp:4
	v_mfma_f32_16x16x128_f8f6f4 v[50:53], v[214:217], v[182:185], v[50:53] cbsz:4 blgp:4
	v_mfma_f32_16x16x128_f8f6f4 v[50:53], v[222:225], v[190:193], v[50:53] cbsz:4 blgp:4
	v_mfma_f32_16x16x128_f8f6f4 v[54:57], v[218:221], v[182:185], v[54:57] cbsz:4 blgp:4
	v_mfma_f32_16x16x128_f8f6f4 v[54:57], v[226:229], v[190:193], v[54:57] cbsz:4 blgp:4
	v_mfma_f32_16x16x128_f8f6f4 v[58:61], v[214:217], v[186:189], v[58:61] cbsz:4 blgp:4
	v_mfma_f32_16x16x128_f8f6f4 v[58:61], v[222:225], v[194:197], v[58:61] cbsz:4 blgp:4
	v_mfma_f32_16x16x128_f8f6f4 v[62:65], v[218:221], v[186:189], v[62:65] cbsz:4 blgp:4
	v_mfma_f32_16x16x128_f8f6f4 v[62:65], v[226:229], v[194:197], v[62:65] cbsz:4 blgp:4
	v_mfma_f32_16x16x128_f8f6f4 v[66:69], v[214:217], v[198:201], v[66:69] cbsz:4 blgp:4
	v_mfma_f32_16x16x128_f8f6f4 v[66:69], v[222:225], v[206:209], v[66:69] cbsz:4 blgp:4
	v_mfma_f32_16x16x128_f8f6f4 v[70:73], v[218:221], v[198:201], v[70:73] cbsz:4 blgp:4
	v_mfma_f32_16x16x128_f8f6f4 v[70:73], v[226:229], v[206:209], v[70:73] cbsz:4 blgp:4
	v_mfma_f32_16x16x128_f8f6f4 v[74:77], v[214:217], v[202:205], v[74:77] cbsz:4 blgp:4
	v_mfma_f32_16x16x128_f8f6f4 v[74:77], v[222:225], v[210:213], v[74:77] cbsz:4 blgp:4
	v_mfma_f32_16x16x128_f8f6f4 v[78:81], v[218:221], v[202:205], v[78:81] cbsz:4 blgp:4
	v_mfma_f32_16x16x128_f8f6f4 v[78:81], v[226:229], v[210:213], v[78:81] cbsz:4 blgp:4
	s_setprio 0
	s_barrier
	s_mov_b32 m0, s54
	s_nop 0
	global_load_lds_dwordx4 v164, s[44:45]
	s_mov_b32 m0, s55
	s_nop 0
	global_load_lds_dwordx4 v168, s[44:45]
	ds_read_b128 v[182:185], v179 offset:16384
	ds_read_b128 v[186:189], v179 offset:18432
	ds_read_b128 v[190:193], v180 offset:16384
	ds_read_b128 v[194:197], v180 offset:18432
	ds_read_b128 v[198:201], v179 offset:20480
	ds_read_b128 v[202:205], v179 offset:22528
	ds_read_b128 v[206:209], v180 offset:20480
	ds_read_b128 v[210:213], v180 offset:22528
	s_mov_b32 m0, s53
	s_nop 0
	global_load_lds_dwordx4 v162, s[42:43]
	s_mov_b32 m0, s56
	s_nop 0
	global_load_lds_dwordx4 v166, s[42:43]
	s_add_u32 s44, s44, s22
	s_addc_u32 s45, s45, s23
	s_mov_b32 m0, s57
	s_nop 0
	global_load_lds_dwordx4 v164, s[44:45]
	s_mov_b32 m0, s58
	s_nop 0
	global_load_lds_dwordx4 v168, s[44:45]
	s_waitcnt vmcnt(8)
	s_waitcnt lgkmcnt(0)
	s_barrier
	s_setprio 1
	v_mfma_f32_16x16x128_f8f6f4 v[86:89], v[146:149], v[182:185], v[86:89] cbsz:4 blgp:4
	v_mfma_f32_16x16x128_f8f6f4 v[86:89], v[154:157], v[190:193], v[86:89] cbsz:4 blgp:4
	v_mfma_f32_16x16x128_f8f6f4 v[90:93], v[150:153], v[182:185], v[90:93] cbsz:4 blgp:4
	v_mfma_f32_16x16x128_f8f6f4 v[90:93], v[158:161], v[190:193], v[90:93] cbsz:4 blgp:4
	v_mfma_f32_16x16x128_f8f6f4 v[98:101], v[146:149], v[186:189], v[98:101] cbsz:4 blgp:4
	v_mfma_f32_16x16x128_f8f6f4 v[98:101], v[154:157], v[194:197], v[98:101] cbsz:4 blgp:4
	v_mfma_f32_16x16x128_f8f6f4 v[106:109], v[150:153], v[186:189], v[106:109] cbsz:4 blgp:4
	v_mfma_f32_16x16x128_f8f6f4 v[106:109], v[158:161], v[194:197], v[106:109] cbsz:4 blgp:4
	v_mfma_f32_16x16x128_f8f6f4 v[118:121], v[146:149], v[198:201], v[118:121] cbsz:4 blgp:4
	v_mfma_f32_16x16x128_f8f6f4 v[118:121], v[154:157], v[206:209], v[118:121] cbsz:4 blgp:4
	v_mfma_f32_16x16x128_f8f6f4 v[126:129], v[150:153], v[198:201], v[126:129] cbsz:4 blgp:4
	v_mfma_f32_16x16x128_f8f6f4 v[126:129], v[158:161], v[206:209], v[126:129] cbsz:4 blgp:4
	v_mfma_f32_16x16x128_f8f6f4 v[138:141], v[146:149], v[202:205], v[138:141] cbsz:4 blgp:4
	v_mfma_f32_16x16x128_f8f6f4 v[138:141], v[154:157], v[210:213], v[138:141] cbsz:4 blgp:4
	v_mfma_f32_16x16x128_f8f6f4 v[82:85], v[150:153], v[202:205], v[82:85] cbsz:4 blgp:4
	v_mfma_f32_16x16x128_f8f6f4 v[82:85], v[158:161], v[210:213], v[82:85] cbsz:4 blgp:4
	v_mfma_f32_16x16x128_f8f6f4 v[94:97], v[214:217], v[182:185], v[94:97] cbsz:4 blgp:4
	v_mfma_f32_16x16x128_f8f6f4 v[94:97], v[222:225], v[190:193], v[94:97] cbsz:4 blgp:4
	v_mfma_f32_16x16x128_f8f6f4 v[102:105], v[218:221], v[182:185], v[102:105] cbsz:4 blgp:4
	v_mfma_f32_16x16x128_f8f6f4 v[102:105], v[226:229], v[190:193], v[102:105] cbsz:4 blgp:4
	v_mfma_f32_16x16x128_f8f6f4 v[110:113], v[214:217], v[186:189], v[110:113] cbsz:4 blgp:4
	v_mfma_f32_16x16x128_f8f6f4 v[110:113], v[222:225], v[194:197], v[110:113] cbsz:4 blgp:4
	v_mfma_f32_16x16x128_f8f6f4 v[114:117], v[218:221], v[186:189], v[114:117] cbsz:4 blgp:4
	v_mfma_f32_16x16x128_f8f6f4 v[114:117], v[226:229], v[194:197], v[114:117] cbsz:4 blgp:4
	v_mfma_f32_16x16x128_f8f6f4 v[122:125], v[214:217], v[198:201], v[122:125] cbsz:4 blgp:4
	v_mfma_f32_16x16x128_f8f6f4 v[122:125], v[222:225], v[206:209], v[122:125] cbsz:4 blgp:4
	v_mfma_f32_16x16x128_f8f6f4 v[130:133], v[218:221], v[198:201], v[130:133] cbsz:4 blgp:4
	v_mfma_f32_16x16x128_f8f6f4 v[130:133], v[226:229], v[206:209], v[130:133] cbsz:4 blgp:4
	v_mfma_f32_16x16x128_f8f6f4 v[134:137], v[214:217], v[202:205], v[134:137] cbsz:4 blgp:4
	v_mfma_f32_16x16x128_f8f6f4 v[134:137], v[222:225], v[210:213], v[134:137] cbsz:4 blgp:4
	v_mfma_f32_16x16x128_f8f6f4 v[142:145], v[218:221], v[202:205], v[142:145] cbsz:4 blgp:4
	v_mfma_f32_16x16x128_f8f6f4 v[142:145], v[226:229], v[210:213], v[142:145] cbsz:4 blgp:4
	s_setprio 0
	s_barrier
	ds_read_b128 v[146:149], v169 offset:32768
	ds_read_b128 v[150:153], v169 offset:34816
	ds_read_b128 v[154:157], v178 offset:32768
	ds_read_b128 v[158:161], v178 offset:34816
	ds_read_b128 v[182:185], v179 offset:32768
	ds_read_b128 v[186:189], v179 offset:34816
	ds_read_b128 v[190:193], v180 offset:32768
	ds_read_b128 v[194:197], v180 offset:34816
	ds_read_b128 v[198:201], v179 offset:36864
	ds_read_b128 v[202:205], v179 offset:38912
	ds_read_b128 v[206:209], v180 offset:36864
	ds_read_b128 v[210:213], v180 offset:38912
	s_add_u32 s42, s42, s20
	s_addc_u32 s43, s43, s21
	s_mov_b32 m0, s59
	s_nop 0
	global_load_lds_dwordx4 v162, s[42:43]
	s_mov_b32 m0, s60
	s_nop 0
	global_load_lds_dwordx4 v166, s[42:43]
	s_waitcnt lgkmcnt(8)
	ds_read_b128 v[214:217], v169 offset:49152
	ds_read_b128 v[218:221], v169 offset:51200
	ds_read_b128 v[222:225], v178 offset:49152
	ds_read_b128 v[226:229], v178 offset:51200
	s_waitcnt vmcnt(8)
	s_waitcnt lgkmcnt(0)
	s_barrier
	s_waitcnt lgkmcnt(0)
	s_setprio 1
	v_mfma_f32_16x16x128_f8f6f4 v[18:21], v[146:149], v[182:185], v[18:21] cbsz:4 blgp:4
	v_mfma_f32_16x16x128_f8f6f4 v[18:21], v[154:157], v[190:193], v[18:21] cbsz:4 blgp:4
	v_mfma_f32_16x16x128_f8f6f4 v[22:25], v[150:153], v[182:185], v[22:25] cbsz:4 blgp:4
	v_mfma_f32_16x16x128_f8f6f4 v[22:25], v[158:161], v[190:193], v[22:25] cbsz:4 blgp:4
	v_mfma_f32_16x16x128_f8f6f4 v[26:29], v[146:149], v[186:189], v[26:29] cbsz:4 blgp:4
	v_mfma_f32_16x16x128_f8f6f4 v[26:29], v[154:157], v[194:197], v[26:29] cbsz:4 blgp:4
	v_mfma_f32_16x16x128_f8f6f4 v[30:33], v[150:153], v[186:189], v[30:33] cbsz:4 blgp:4
	v_mfma_f32_16x16x128_f8f6f4 v[30:33], v[158:161], v[194:197], v[30:33] cbsz:4 blgp:4
	v_mfma_f32_16x16x128_f8f6f4 v[34:37], v[146:149], v[198:201], v[34:37] cbsz:4 blgp:4
	v_mfma_f32_16x16x128_f8f6f4 v[34:37], v[154:157], v[206:209], v[34:37] cbsz:4 blgp:4
	v_mfma_f32_16x16x128_f8f6f4 v[38:41], v[150:153], v[198:201], v[38:41] cbsz:4 blgp:4
	v_mfma_f32_16x16x128_f8f6f4 v[38:41], v[158:161], v[206:209], v[38:41] cbsz:4 blgp:4
	v_mfma_f32_16x16x128_f8f6f4 v[42:45], v[146:149], v[202:205], v[42:45] cbsz:4 blgp:4
	v_mfma_f32_16x16x128_f8f6f4 v[42:45], v[154:157], v[210:213], v[42:45] cbsz:4 blgp:4
	v_mfma_f32_16x16x128_f8f6f4 v[46:49], v[150:153], v[202:205], v[46:49] cbsz:4 blgp:4
	v_mfma_f32_16x16x128_f8f6f4 v[46:49], v[158:161], v[210:213], v[46:49] cbsz:4 blgp:4
	v_mfma_f32_16x16x128_f8f6f4 v[50:53], v[214:217], v[182:185], v[50:53] cbsz:4 blgp:4
	v_mfma_f32_16x16x128_f8f6f4 v[50:53], v[222:225], v[190:193], v[50:53] cbsz:4 blgp:4
	v_mfma_f32_16x16x128_f8f6f4 v[54:57], v[218:221], v[182:185], v[54:57] cbsz:4 blgp:4
	v_mfma_f32_16x16x128_f8f6f4 v[54:57], v[226:229], v[190:193], v[54:57] cbsz:4 blgp:4
	v_mfma_f32_16x16x128_f8f6f4 v[58:61], v[214:217], v[186:189], v[58:61] cbsz:4 blgp:4
	v_mfma_f32_16x16x128_f8f6f4 v[58:61], v[222:225], v[194:197], v[58:61] cbsz:4 blgp:4
	v_mfma_f32_16x16x128_f8f6f4 v[62:65], v[218:221], v[186:189], v[62:65] cbsz:4 blgp:4
	v_mfma_f32_16x16x128_f8f6f4 v[62:65], v[226:229], v[194:197], v[62:65] cbsz:4 blgp:4
	v_mfma_f32_16x16x128_f8f6f4 v[66:69], v[214:217], v[198:201], v[66:69] cbsz:4 blgp:4
	v_mfma_f32_16x16x128_f8f6f4 v[66:69], v[222:225], v[206:209], v[66:69] cbsz:4 blgp:4
	v_mfma_f32_16x16x128_f8f6f4 v[70:73], v[218:221], v[198:201], v[70:73] cbsz:4 blgp:4
	v_mfma_f32_16x16x128_f8f6f4 v[70:73], v[226:229], v[206:209], v[70:73] cbsz:4 blgp:4
	v_mfma_f32_16x16x128_f8f6f4 v[74:77], v[214:217], v[202:205], v[74:77] cbsz:4 blgp:4
	v_mfma_f32_16x16x128_f8f6f4 v[74:77], v[222:225], v[210:213], v[74:77] cbsz:4 blgp:4
	v_mfma_f32_16x16x128_f8f6f4 v[78:81], v[218:221], v[202:205], v[78:81] cbsz:4 blgp:4
	v_mfma_f32_16x16x128_f8f6f4 v[78:81], v[226:229], v[210:213], v[78:81] cbsz:4 blgp:4
	s_setprio 0
	s_barrier
	s_mov_b32 m0, s62
	s_nop 0
	global_load_lds_dwordx4 v164, s[36:37]
	s_mov_b32 m0, s63
	s_nop 0
	global_load_lds_dwordx4 v168, s[36:37]
	ds_read_b128 v[182:185], v179 offset:49152
	ds_read_b128 v[186:189], v179 offset:51200
	ds_read_b128 v[190:193], v180 offset:49152
	ds_read_b128 v[194:197], v180 offset:51200
	ds_read_b128 v[198:201], v179 offset:53248
	ds_read_b128 v[202:205], v179 offset:55296
	ds_read_b128 v[206:209], v180 offset:53248
	ds_read_b128 v[210:213], v180 offset:55296
	s_mov_b32 m0, s64
	s_nop 0
	global_load_lds_dwordx4 v162, s[40:41]
	s_mov_b32 m0, s65
	s_nop 0
	global_load_lds_dwordx4 v166, s[40:41]
	s_add_u32 s36, s36, s22
	s_addc_u32 s37, s37, s23
	s_mov_b32 m0, s66
	s_nop 0
	global_load_lds_dwordx4 v164, s[36:37]
	s_mov_b32 m0, s67
	s_nop 0
	global_load_lds_dwordx4 v168, s[36:37]
	s_waitcnt vmcnt(8)
	s_waitcnt lgkmcnt(0)
	s_barrier
	s_setprio 1
	v_mfma_f32_16x16x128_f8f6f4 v[86:89], v[146:149], v[182:185], v[86:89] cbsz:4 blgp:4
	v_mfma_f32_16x16x128_f8f6f4 v[86:89], v[154:157], v[190:193], v[86:89] cbsz:4 blgp:4
	v_mfma_f32_16x16x128_f8f6f4 v[90:93], v[150:153], v[182:185], v[90:93] cbsz:4 blgp:4
	v_mfma_f32_16x16x128_f8f6f4 v[90:93], v[158:161], v[190:193], v[90:93] cbsz:4 blgp:4
	v_mfma_f32_16x16x128_f8f6f4 v[98:101], v[146:149], v[186:189], v[98:101] cbsz:4 blgp:4
	v_mfma_f32_16x16x128_f8f6f4 v[98:101], v[154:157], v[194:197], v[98:101] cbsz:4 blgp:4
	v_mfma_f32_16x16x128_f8f6f4 v[106:109], v[150:153], v[186:189], v[106:109] cbsz:4 blgp:4
	v_mfma_f32_16x16x128_f8f6f4 v[106:109], v[158:161], v[194:197], v[106:109] cbsz:4 blgp:4
	v_mfma_f32_16x16x128_f8f6f4 v[118:121], v[146:149], v[198:201], v[118:121] cbsz:4 blgp:4
	v_mfma_f32_16x16x128_f8f6f4 v[118:121], v[154:157], v[206:209], v[118:121] cbsz:4 blgp:4
	v_mfma_f32_16x16x128_f8f6f4 v[126:129], v[150:153], v[198:201], v[126:129] cbsz:4 blgp:4
	v_mfma_f32_16x16x128_f8f6f4 v[126:129], v[158:161], v[206:209], v[126:129] cbsz:4 blgp:4
	v_mfma_f32_16x16x128_f8f6f4 v[138:141], v[146:149], v[202:205], v[138:141] cbsz:4 blgp:4
	v_mfma_f32_16x16x128_f8f6f4 v[138:141], v[154:157], v[210:213], v[138:141] cbsz:4 blgp:4
	v_mfma_f32_16x16x128_f8f6f4 v[82:85], v[150:153], v[202:205], v[82:85] cbsz:4 blgp:4
	v_mfma_f32_16x16x128_f8f6f4 v[82:85], v[158:161], v[210:213], v[82:85] cbsz:4 blgp:4
	v_mfma_f32_16x16x128_f8f6f4 v[94:97], v[214:217], v[182:185], v[94:97] cbsz:4 blgp:4
	v_mfma_f32_16x16x128_f8f6f4 v[94:97], v[222:225], v[190:193], v[94:97] cbsz:4 blgp:4
	v_mfma_f32_16x16x128_f8f6f4 v[102:105], v[218:221], v[182:185], v[102:105] cbsz:4 blgp:4
	v_mfma_f32_16x16x128_f8f6f4 v[102:105], v[226:229], v[190:193], v[102:105] cbsz:4 blgp:4
	v_mfma_f32_16x16x128_f8f6f4 v[110:113], v[214:217], v[186:189], v[110:113] cbsz:4 blgp:4
	v_mfma_f32_16x16x128_f8f6f4 v[110:113], v[222:225], v[194:197], v[110:113] cbsz:4 blgp:4
	v_mfma_f32_16x16x128_f8f6f4 v[114:117], v[218:221], v[186:189], v[114:117] cbsz:4 blgp:4
	v_mfma_f32_16x16x128_f8f6f4 v[114:117], v[226:229], v[194:197], v[114:117] cbsz:4 blgp:4
	v_mfma_f32_16x16x128_f8f6f4 v[122:125], v[214:217], v[198:201], v[122:125] cbsz:4 blgp:4
	v_mfma_f32_16x16x128_f8f6f4 v[122:125], v[222:225], v[206:209], v[122:125] cbsz:4 blgp:4
	v_mfma_f32_16x16x128_f8f6f4 v[130:133], v[218:221], v[198:201], v[130:133] cbsz:4 blgp:4
	v_mfma_f32_16x16x128_f8f6f4 v[130:133], v[226:229], v[206:209], v[130:133] cbsz:4 blgp:4
	v_mfma_f32_16x16x128_f8f6f4 v[134:137], v[214:217], v[202:205], v[134:137] cbsz:4 blgp:4
	v_mfma_f32_16x16x128_f8f6f4 v[134:137], v[222:225], v[210:213], v[134:137] cbsz:4 blgp:4
	v_mfma_f32_16x16x128_f8f6f4 v[142:145], v[218:221], v[202:205], v[142:145] cbsz:4 blgp:4
	v_mfma_f32_16x16x128_f8f6f4 v[142:145], v[226:229], v[210:213], v[142:145] cbsz:4 blgp:4
	s_setprio 0
	s_add_i32 s36, s82, 2
	s_add_u32 s31, s31, 0x100
	s_addc_u32 s46, s46, 0
	s_add_u32 s47, s47, 0x100
	s_addc_u32 s81, s81, 0
	s_add_u32 s34, s34, 0x100
	s_addc_u32 s35, s35, 0
	s_cmp_ge_i32 s82, s61
	s_barrier
	s_cbranch_scc1 .LBB6_20
	s_mov_b32 s82, s36
	s_cmp_eq_u32 s61, s82
	s_cselect_b64 s[36:37], -1, 0
	s_cmp_lg_u32 s61, s82
	s_cbranch_scc0 .LBB6_17
	s_branch .LBB6_18
